# row phases with 8x2048 gate/router dot products: the 64 per-row LDS weight reads hoisted 12-deep into unused registers, counted lgkmcnt waits
# speedup vs baseline: 1.0059x; 1.0059x over previous
; #define LAS __attribute__((address_space(3)))
; __device__ __forceinline__ unsigned cvtpk(float lo, float hi) { f32x2 v = {lo, hi}; bf16x2_t b = __builtin_convertvector(v, bf16x2_t); return __builtin_bit_cast(unsigned, b); }
; __device__ __forceinline__ float wave_sum(float v) { return lane63(scan64<false>(v)); }
; __device__ __forceinline__ float wave_max(float v) { return lane63(scan64<true>(v)); }
; template <int YMODE, int EXTRA, bool NORM_OUT, bool XN8  , bool XIN_BF = false  , bool XOUT_BF = false  > ...
;     ...
;                 if (XN8) {
;                     float am = 0.f;
; #pragma unroll
;                     for (int j = 0; j < 8; ++j) am = fmaxf(fmaxf(am, fmaxf(fabsf(x[j][0]), fabsf(x[j][1]))), fmaxf(fabsf(x[j][2]), fabsf(x[j][3])));
;                     am = wave_max(am);
;                     const float inv = am > 0.f ? 127.f / am : 0.f;
;                     if (F.lane == 0) { rowmax[row] = am; if (EXTRA == 2) route[384 + rl] = am; }
; #pragma unroll
;                     for (int j = 0; j < 8; ++j) *(unsigned*)((unsigned char*)XN + row * D + 256 * j + 4 * F.lane) = pack_i8x4(x[j][0] * inv, x[j][1] * inv, x[j][2] * inv, x[j][3] * inv);
;                 } else {
; #pragma unroll
;                     for (int j = 0; j < 8; ++j) { u32x2 w; w.x = cvtpk(x[j][0], x[j][1]); w.y = cvtpk(x[j][2], x[j][3]); *(u32x2*)(XN + row * D + 256 * j + 4 * F.lane) = w; }
;                 }
;                 if (EXTRA) {
;                     float d8[8];
; #pragma unroll
;                     for (int e = 0; e < 8; ++e) { float s = 0.f;
; #pragma unroll
;                         for (int j = 0; j < 8; ++j) { const f32x4 w = *(const LAS f32x4*)(we + e * D + 256 * j + 4 * F.lane); s += (x[j][0] * w[0] + x[j][1] * w[1]) + (x[j][2] * w[2] + x[j][3] * w[3]); }
;                         d8[e] = wave_sum(s); asm volatile("" ::: "memory"); }
.LBB0_112:
	s_or_b64 exec, exec, s[36:37]
	ds_read_b128 v[196:199], v88
	ds_read_b128 v[200:203], v88 offset:1024
	ds_read_b128 v[204:207], v88 offset:2048
	ds_read_b128 v[208:211], v88 offset:3072
	ds_read_b128 v[212:215], v88 offset:4096
	ds_read_b128 v[216:219], v88 offset:5120
	ds_read_b128 v[220:223], v88 offset:6144
	ds_read_b128 v[224:227], v88 offset:7168
	ds_read_b128 v[228:231], v88 offset:8192
	ds_read_b128 v[232:235], v88 offset:9216
	ds_read_b128 v[240:243], v88 offset:10240
	ds_read_b128 v[244:247], v88 offset:11264
	v_div_scale_f32 v1, s[36:37], s34, s34, v93
	v_rcp_f32_e32 v83, v1
	v_mov_b32_e32 v95, s34
	v_div_scale_f32 v95, vcc, s40, v95, s40
	v_fma_f32 v96, -v1, v83, 1.0
	v_fmac_f32_e32 v83, v96, v83
	v_mul_f32_e32 v96, v95, v83
	v_fma_f32 v97, -v1, v96, v95
	v_fmac_f32_e32 v96, v97, v83
	v_fma_f32 v1, -v1, v96, v95
	v_div_fmas_f32 v1, v1, v83, v96
	v_div_fixup_f32 v1, v1, s34, v93
	v_cmp_gt_f32_e64 vcc, s34, 0
	s_lshl_b64 s[36:37], s[26:27], 11
	v_lshl_add_u64 v[100:101], v[80:81], 0, s[36:37]
	v_cndmask_b32_e32 v1, 0, v1, vcc
	v_mul_f32_e32 v95, v65, v1
	v_mul_f32_e32 v83, v64, v1
	v_mul_f32_e32 v96, v62, v1
	v_mul_f32_e32 v97, v63, v1
	v_med3_f32 v95, v95, s41, v93
	v_med3_f32 v83, v83, s41, v93
	v_rndne_f32_e32 v95, v95
	v_med3_f32 v96, v96, s41, v93
	v_med3_f32 v97, v97, s41, v93
	v_rndne_f32_e32 v83, v83
	v_cvt_i32_f32_e32 v95, v95
	v_rndne_f32_e32 v96, v96
	v_rndne_f32_e32 v97, v97
	v_cvt_i32_f32_e32 v83, v83
	v_cvt_i32_f32_sdwa v96, v96 dst_sel:WORD_1 dst_unused:UNUSED_PAD src0_sel:DWORD
	v_cvt_i32_f32_e32 v97, v97
	v_lshlrev_b32_e32 v95, 8, v95
	v_and_b32_e32 v95, 0xff00, v95
	v_and_b32_e32 v96, 0xff0000, v96
	v_perm_b32 v83, v97, v83, s42
	v_or3_b32 v83, v83, v95, v96
	v_mul_f32_e32 v95, v61, v1
	global_store_dword v[100:101], v83, off
	v_mul_f32_e32 v83, v60, v1
	v_mul_f32_e32 v96, v58, v1
	v_mul_f32_e32 v97, v59, v1
	v_med3_f32 v95, v95, s41, v93
	v_med3_f32 v83, v83, s41, v93
	v_rndne_f32_e32 v95, v95
	v_med3_f32 v96, v96, s41, v93
	v_med3_f32 v97, v97, s41, v93
	v_rndne_f32_e32 v83, v83
	v_cvt_i32_f32_e32 v95, v95
	v_rndne_f32_e32 v96, v96
	v_rndne_f32_e32 v97, v97
	v_cvt_i32_f32_e32 v83, v83
	v_cvt_i32_f32_sdwa v96, v96 dst_sel:WORD_1 dst_unused:UNUSED_PAD src0_sel:DWORD
	v_cvt_i32_f32_e32 v97, v97
	v_lshlrev_b32_e32 v95, 8, v95
	v_and_b32_e32 v95, 0xff00, v95
	v_and_b32_e32 v96, 0xff0000, v96
	v_perm_b32 v83, v97, v83, s42
	v_or3_b32 v83, v83, v95, v96
	v_mul_f32_e32 v95, v57, v1
	global_store_dword v[100:101], v83, off offset:256
	v_mul_f32_e32 v83, v56, v1
	v_mul_f32_e32 v96, v54, v1
	v_mul_f32_e32 v97, v55, v1
	v_med3_f32 v95, v95, s41, v93
	v_med3_f32 v83, v83, s41, v93
	v_rndne_f32_e32 v95, v95
	v_med3_f32 v96, v96, s41, v93
	v_med3_f32 v97, v97, s41, v93
	v_rndne_f32_e32 v83, v83
	v_cvt_i32_f32_e32 v95, v95
	v_rndne_f32_e32 v96, v96
	v_rndne_f32_e32 v97, v97
	v_cvt_i32_f32_e32 v83, v83
	v_cvt_i32_f32_sdwa v96, v96 dst_sel:WORD_1 dst_unused:UNUSED_PAD src0_sel:DWORD
	v_cvt_i32_f32_e32 v97, v97
	v_lshlrev_b32_e32 v95, 8, v95
	v_and_b32_e32 v95, 0xff00, v95
	v_and_b32_e32 v96, 0xff0000, v96
	v_perm_b32 v83, v97, v83, s42
	v_or3_b32 v83, v83, v95, v96
	v_mul_f32_e32 v95, v53, v1
	global_store_dword v[100:101], v83, off offset:512
	v_mul_f32_e32 v83, v52, v1
	v_mul_f32_e32 v96, v50, v1
	v_mul_f32_e32 v97, v51, v1
	v_med3_f32 v95, v95, s41, v93
	v_med3_f32 v83, v83, s41, v93
	v_rndne_f32_e32 v95, v95
	v_med3_f32 v96, v96, s41, v93
	v_med3_f32 v97, v97, s41, v93
	v_rndne_f32_e32 v83, v83
	v_cvt_i32_f32_e32 v95, v95
	v_rndne_f32_e32 v96, v96
	v_rndne_f32_e32 v97, v97
	v_cvt_i32_f32_e32 v83, v83
	v_cvt_i32_f32_sdwa v96, v96 dst_sel:WORD_1 dst_unused:UNUSED_PAD src0_sel:DWORD
	v_cvt_i32_f32_e32 v97, v97
	v_lshlrev_b32_e32 v95, 8, v95
	v_and_b32_e32 v95, 0xff00, v95
	v_and_b32_e32 v96, 0xff0000, v96
	v_perm_b32 v83, v97, v83, s42
	v_or3_b32 v83, v83, v95, v96
	v_mul_f32_e32 v95, v49, v1
	global_store_dword v[100:101], v83, off offset:768
	v_mul_f32_e32 v83, v48, v1
	v_mul_f32_e32 v96, v46, v1
	v_mul_f32_e32 v97, v47, v1
	v_med3_f32 v95, v95, s41, v93
	v_med3_f32 v83, v83, s41, v93
	v_rndne_f32_e32 v95, v95
	v_med3_f32 v96, v96, s41, v93
	v_med3_f32 v97, v97, s41, v93
	v_rndne_f32_e32 v83, v83
	v_cvt_i32_f32_e32 v95, v95
	v_rndne_f32_e32 v96, v96
	v_rndne_f32_e32 v97, v97
	v_cvt_i32_f32_e32 v83, v83
	v_cvt_i32_f32_sdwa v96, v96 dst_sel:WORD_1 dst_unused:UNUSED_PAD src0_sel:DWORD
	v_cvt_i32_f32_e32 v97, v97
	v_lshlrev_b32_e32 v95, 8, v95
	v_and_b32_e32 v95, 0xff00, v95
	v_and_b32_e32 v96, 0xff0000, v96
	v_perm_b32 v83, v97, v83, s42
	v_or3_b32 v83, v83, v95, v96
	v_mul_f32_e32 v95, v45, v1
	global_store_dword v[100:101], v83, off offset:1024
	v_mul_f32_e32 v83, v44, v1
	v_mul_f32_e32 v96, v42, v1
	v_mul_f32_e32 v97, v43, v1
	v_med3_f32 v95, v95, s41, v93
	v_med3_f32 v83, v83, s41, v93
	v_rndne_f32_e32 v95, v95
	v_med3_f32 v96, v96, s41, v93
	v_med3_f32 v97, v97, s41, v93
	v_rndne_f32_e32 v83, v83
	v_cvt_i32_f32_e32 v95, v95
	v_rndne_f32_e32 v96, v96
	v_rndne_f32_e32 v97, v97
	v_cvt_i32_f32_e32 v83, v83
	v_cvt_i32_f32_sdwa v96, v96 dst_sel:WORD_1 dst_unused:UNUSED_PAD src0_sel:DWORD
	v_cvt_i32_f32_e32 v97, v97
	v_lshlrev_b32_e32 v95, 8, v95
	v_and_b32_e32 v95, 0xff00, v95
	v_and_b32_e32 v96, 0xff0000, v96
	v_perm_b32 v83, v97, v83, s42
	v_or3_b32 v83, v83, v95, v96
	v_mul_f32_e32 v95, v41, v1
	global_store_dword v[100:101], v83, off offset:1280
	v_mul_f32_e32 v83, v40, v1
	v_mul_f32_e32 v96, v38, v1
	v_mul_f32_e32 v97, v39, v1
	v_med3_f32 v95, v95, s41, v93
	v_med3_f32 v83, v83, s41, v93
	v_rndne_f32_e32 v95, v95
	v_med3_f32 v96, v96, s41, v93
	v_med3_f32 v97, v97, s41, v93
	v_rndne_f32_e32 v83, v83
	v_cvt_i32_f32_e32 v95, v95
	v_rndne_f32_e32 v96, v96
	v_rndne_f32_e32 v97, v97
	v_cvt_i32_f32_e32 v83, v83
	v_cvt_i32_f32_sdwa v96, v96 dst_sel:WORD_1 dst_unused:UNUSED_PAD src0_sel:DWORD
	v_cvt_i32_f32_e32 v97, v97
	v_lshlrev_b32_e32 v95, 8, v95
	v_and_b32_e32 v95, 0xff00, v95
	v_and_b32_e32 v96, 0xff0000, v96
	v_perm_b32 v83, v97, v83, s42
	v_or3_b32 v83, v83, v95, v96
	v_mul_f32_e32 v95, v37, v1
	v_mul_f32_e32 v96, v34, v1
	global_store_dword v[100:101], v83, off offset:1536
	v_mul_f32_e32 v83, v36, v1
	v_mul_f32_e32 v1, v35, v1
	v_med3_f32 v95, v95, s41, v93
	v_med3_f32 v96, v96, s41, v93
	v_med3_f32 v83, v83, s41, v93
	v_rndne_f32_e32 v95, v95
	v_rndne_f32_e32 v96, v96
	v_med3_f32 v1, v1, s41, v93
	v_rndne_f32_e32 v83, v83
	v_cvt_i32_f32_e32 v95, v95
	v_cvt_i32_f32_sdwa v96, v96 dst_sel:WORD_1 dst_unused:UNUSED_PAD src0_sel:DWORD
	v_rndne_f32_e32 v1, v1
	v_cvt_i32_f32_e32 v83, v83
	v_cvt_i32_f32_e32 v1, v1
	v_lshlrev_b32_e32 v95, 8, v95
	v_and_b32_e32 v102, 0xff0000, v96
	s_nop 0
	v_and_b32_e32 v95, 0xff00, v95
	v_perm_b32 v1, v1, v83, s42
	v_or3_b32 v1, v1, v95, v102
	global_store_dword v[100:101], v1, off offset:1792
	s_nop 0
	s_waitcnt lgkmcnt(12)
; #define LAS __attribute__((address_space(3)))
; __device__ __forceinline__ float wave_sum(float v) { return lane63(scan64<false>(v)); }
; template <int YMODE, int EXTRA, bool NORM_OUT, bool XN8  , bool XIN_BF = false  , bool XOUT_BF = false  > ...
;     ...
;                 if (EXTRA) {
;                     float d8[8];
; #pragma unroll
;                     for (int e = 0; e < 8; ++e) { float s = 0.f;
; #pragma unroll
;                         for (int j = 0; j < 8; ++j) { const f32x4 w = *(const LAS f32x4*)(we + e * D + 256 * j + 4 * F.lane); s += (x[j][0] * w[0] + x[j][1] * w[1]) + (x[j][2] * w[2] + x[j][3] * w[3]); }
;                         d8[e] = wave_sum(s); asm volatile("" ::: "memory"); }
	s_waitcnt lgkmcnt(11)
	v_mul_f32_e32 v1, v65, v197
	ds_read_b128 v[248:251], v88 offset:12288
	v_mul_f32_e32 v83, v63, v199
	v_fmac_f32_e32 v1, v64, v196
	v_fmac_f32_e32 v83, v62, v198
	v_add_f32_e32 v1, v1, v83
	s_waitcnt lgkmcnt(11)
	v_mul_f32_e32 v83, v61, v201
	ds_read_b128 v[196:199], v88 offset:13312
	v_mul_f32_e32 v95, v59, v203
	v_fmac_f32_e32 v83, v60, v200
	v_fmac_f32_e32 v95, v58, v202
	v_add_f32_e32 v1, 0, v1
	v_add_f32_e32 v83, v83, v95
	v_add_f32_e32 v1, v1, v83
	s_waitcnt lgkmcnt(11)
	v_mul_f32_e32 v83, v57, v205
	ds_read_b128 v[200:203], v88 offset:14336
	v_mul_f32_e32 v95, v55, v207
	v_fmac_f32_e32 v83, v56, v204
	v_fmac_f32_e32 v95, v54, v206
	v_add_f32_e32 v83, v83, v95
	v_add_f32_e32 v1, v1, v83
	s_waitcnt lgkmcnt(11)
	v_mul_f32_e32 v83, v53, v209
	ds_read_b128 v[204:207], v88 offset:15360
	v_mul_f32_e32 v95, v51, v211
	v_fmac_f32_e32 v83, v52, v208
	v_fmac_f32_e32 v95, v50, v210
	v_add_f32_e32 v83, v83, v95
	v_add_f32_e32 v1, v1, v83
	s_waitcnt lgkmcnt(11)
	v_mul_f32_e32 v83, v49, v213
	ds_read_b128 v[208:211], v88 offset:16384
	v_mul_f32_e32 v95, v47, v215
	v_fmac_f32_e32 v83, v48, v212
	v_fmac_f32_e32 v95, v46, v214
	v_add_f32_e32 v83, v83, v95
	v_add_f32_e32 v1, v1, v83
	s_waitcnt lgkmcnt(11)
	v_mul_f32_e32 v83, v45, v217
	ds_read_b128 v[212:215], v88 offset:17408
	v_mul_f32_e32 v95, v43, v219
	v_fmac_f32_e32 v83, v44, v216
	v_fmac_f32_e32 v95, v42, v218
	v_add_f32_e32 v83, v83, v95
	v_add_f32_e32 v1, v1, v83
	s_waitcnt lgkmcnt(11)
	v_mul_f32_e32 v83, v41, v221
	ds_read_b128 v[216:219], v88 offset:18432
	v_mul_f32_e32 v95, v39, v223
	v_fmac_f32_e32 v83, v40, v220
	v_fmac_f32_e32 v95, v38, v222
	v_add_f32_e32 v83, v83, v95
	v_add_f32_e32 v1, v1, v83
	s_waitcnt lgkmcnt(11)
	v_mul_f32_e32 v83, v37, v225
	ds_read_b128 v[220:223], v88 offset:19456
	v_mul_f32_e32 v95, v35, v227
	v_fmac_f32_e32 v83, v36, v224
	v_fmac_f32_e32 v95, v34, v226
	v_add_f32_e32 v83, v83, v95
	v_add_f32_e32 v1, v1, v83
	v_mov_b32_e32 v83, 0
	s_nop 0
	s_nop 0
	v_add_f32_dpp v1, v1, v1 row_shr:1 row_mask:0xf bank_mask:0xf bound_ctrl:1
	s_nop 0
	s_waitcnt lgkmcnt(10)
	v_mul_f32_e32 v95, v59, v235
	ds_read_b128 v[224:227], v88 offset:20480
	v_add_f32_dpp v1, v1, v1 row_shr:2 row_mask:0xf bank_mask:0xf bound_ctrl:1
	v_fmac_f32_e32 v95, v58, v234
	s_nop 0
	v_add_f32_dpp v1, v1, v1 row_shr:4 row_mask:0xf bank_mask:0xf bound_ctrl:1
	s_nop 1
	v_add_f32_dpp v1, v1, v1 row_shr:8 row_mask:0xf bank_mask:0xf bound_ctrl:1
	s_nop 1
	v_mov_b32_dpp v83, v1 row_bcast:15 row_mask:0xa bank_mask:0xf
	v_add_f32_e32 v1, v1, v83
	v_mov_b32_e32 v83, 0
	s_nop 1
	v_mov_b32_dpp v83, v1 row_bcast:31 row_mask:0xc bank_mask:0xf
	v_add_f32_e32 v1, v1, v83
	v_mul_f32_e32 v83, v63, v231
	v_readlane_b32 s34, v1, 63
	v_mul_f32_e32 v1, v65, v229
	v_fmac_f32_e32 v1, v64, v228
	v_fmac_f32_e32 v83, v62, v230
	ds_read_b128 v[228:231], v88 offset:21504
	v_add_f32_e32 v1, v1, v83
	v_mul_f32_e32 v83, v61, v233
	v_fmac_f32_e32 v83, v60, v232
	v_add_f32_e32 v1, 0, v1
	v_add_f32_e32 v83, v83, v95
	v_add_f32_e32 v1, v1, v83
	s_waitcnt lgkmcnt(11)
	v_mul_f32_e32 v83, v57, v241
	ds_read_b128 v[232:235], v88 offset:22528
	v_mul_f32_e32 v95, v55, v243
	v_fmac_f32_e32 v83, v56, v240
	v_fmac_f32_e32 v95, v54, v242
	v_add_f32_e32 v83, v83, v95
	v_add_f32_e32 v1, v1, v83
	s_waitcnt lgkmcnt(11)
	v_mul_f32_e32 v83, v53, v245
	ds_read_b128 v[240:243], v88 offset:23552
	v_mul_f32_e32 v95, v51, v247
	v_fmac_f32_e32 v83, v52, v244
	v_fmac_f32_e32 v95, v50, v246
	v_add_f32_e32 v83, v83, v95
	v_add_f32_e32 v1, v1, v83
	s_waitcnt lgkmcnt(11)
	v_mul_f32_e32 v83, v49, v249
	ds_read_b128 v[244:247], v88 offset:24576
	v_mul_f32_e32 v95, v47, v251
	v_fmac_f32_e32 v83, v48, v248
	v_fmac_f32_e32 v95, v46, v250
	v_add_f32_e32 v83, v83, v95
	v_add_f32_e32 v1, v1, v83
	s_waitcnt lgkmcnt(11)
	v_mul_f32_e32 v83, v45, v197
	ds_read_b128 v[248:251], v88 offset:25600
	v_mul_f32_e32 v95, v43, v199
	v_fmac_f32_e32 v83, v44, v196
	v_fmac_f32_e32 v95, v42, v198
	v_add_f32_e32 v83, v83, v95
	v_add_f32_e32 v1, v1, v83
	s_waitcnt lgkmcnt(11)
	v_mul_f32_e32 v83, v41, v201
	ds_read_b128 v[196:199], v88 offset:26624
	v_mul_f32_e32 v95, v39, v203
	v_fmac_f32_e32 v83, v40, v200
	v_fmac_f32_e32 v95, v38, v202
	v_add_f32_e32 v83, v83, v95
	v_add_f32_e32 v1, v1, v83
	s_waitcnt lgkmcnt(11)
	v_mul_f32_e32 v83, v37, v205
	ds_read_b128 v[200:203], v88 offset:27648
	v_mul_f32_e32 v95, v35, v207
	v_fmac_f32_e32 v83, v36, v204
	v_fmac_f32_e32 v95, v34, v206
	v_add_f32_e32 v83, v83, v95
	v_add_f32_e32 v1, v1, v83
	v_mov_b32_e32 v83, 0
	s_nop 0
	s_nop 0
	v_add_f32_dpp v1, v1, v1 row_shr:1 row_mask:0xf bank_mask:0xf bound_ctrl:1
	s_nop 0
	s_waitcnt lgkmcnt(10)
	v_mul_f32_e32 v95, v59, v215
	ds_read_b128 v[204:207], v88 offset:28672
	v_add_f32_dpp v1, v1, v1 row_shr:2 row_mask:0xf bank_mask:0xf bound_ctrl:1
	v_fmac_f32_e32 v95, v58, v214
	s_nop 0
	v_add_f32_dpp v1, v1, v1 row_shr:4 row_mask:0xf bank_mask:0xf bound_ctrl:1
	s_nop 1
	v_add_f32_dpp v1, v1, v1 row_shr:8 row_mask:0xf bank_mask:0xf bound_ctrl:1
	s_nop 1
	v_mov_b32_dpp v83, v1 row_bcast:15 row_mask:0xa bank_mask:0xf
	v_add_f32_e32 v1, v1, v83
	v_mov_b32_e32 v83, 0
	s_nop 1
	v_mov_b32_dpp v83, v1 row_bcast:31 row_mask:0xc bank_mask:0xf
	v_add_f32_e32 v1, v1, v83
	v_mul_f32_e32 v83, v63, v211
	v_readlane_b32 s38, v1, 63
	v_mul_f32_e32 v1, v65, v209
	v_fmac_f32_e32 v1, v64, v208
	v_fmac_f32_e32 v83, v62, v210
	ds_read_b128 v[208:211], v88 offset:29696
	v_add_f32_e32 v1, v1, v83
	v_mul_f32_e32 v83, v61, v213
	v_fmac_f32_e32 v83, v60, v212
	v_add_f32_e32 v1, 0, v1
	v_add_f32_e32 v83, v83, v95
	v_add_f32_e32 v1, v1, v83
	s_waitcnt lgkmcnt(11)
; #define LAS __attribute__((address_space(3)))
; __device__ __forceinline__ float wave_sum(float v) { return lane63(scan64<false>(v)); }
; template <int YMODE, int EXTRA, bool NORM_OUT, bool XN8  , bool XIN_BF = false  , bool XOUT_BF = false  > ...
;     ...
;                 if (EXTRA) {
;                     float d8[8];
; #pragma unroll
;                     for (int e = 0; e < 8; ++e) { float s = 0.f;
; #pragma unroll
;                         for (int j = 0; j < 8; ++j) { const f32x4 w = *(const LAS f32x4*)(we + e * D + 256 * j + 4 * F.lane); s += (x[j][0] * w[0] + x[j][1] * w[1]) + (x[j][2] * w[2] + x[j][3] * w[3]); }
;                         d8[e] = wave_sum(s); asm volatile("" ::: "memory"); }
	v_mul_f32_e32 v83, v57, v217
	ds_read_b128 v[212:215], v88 offset:30720
	v_mul_f32_e32 v95, v55, v219
	v_fmac_f32_e32 v83, v56, v216
	v_fmac_f32_e32 v95, v54, v218
	v_add_f32_e32 v83, v83, v95
	v_add_f32_e32 v1, v1, v83
	s_waitcnt lgkmcnt(11)
	v_mul_f32_e32 v83, v53, v221
	ds_read_b128 v[216:219], v88 offset:31744
	v_mul_f32_e32 v95, v51, v223
	v_fmac_f32_e32 v83, v52, v220
	v_fmac_f32_e32 v95, v50, v222
	v_add_f32_e32 v83, v83, v95
	v_add_f32_e32 v1, v1, v83
	s_waitcnt lgkmcnt(11)
	v_mul_f32_e32 v83, v49, v225
	ds_read_b128 v[220:223], v88 offset:32768
	v_mul_f32_e32 v95, v47, v227
	v_fmac_f32_e32 v83, v48, v224
	v_fmac_f32_e32 v95, v46, v226
	v_add_f32_e32 v83, v83, v95
	v_add_f32_e32 v1, v1, v83
	s_waitcnt lgkmcnt(11)
	v_mul_f32_e32 v83, v45, v229
	ds_read_b128 v[224:227], v88 offset:33792
	v_mul_f32_e32 v95, v43, v231
	v_fmac_f32_e32 v83, v44, v228
	v_fmac_f32_e32 v95, v42, v230
	v_add_f32_e32 v83, v83, v95
	v_add_f32_e32 v1, v1, v83
	s_waitcnt lgkmcnt(11)
	v_mul_f32_e32 v83, v41, v233
	ds_read_b128 v[228:231], v88 offset:34816
	v_mul_f32_e32 v95, v39, v235
	v_fmac_f32_e32 v83, v40, v232
	v_fmac_f32_e32 v95, v38, v234
	v_add_f32_e32 v83, v83, v95
	v_add_f32_e32 v1, v1, v83
	s_waitcnt lgkmcnt(11)
	v_mul_f32_e32 v83, v37, v241
	ds_read_b128 v[232:235], v88 offset:35840
	v_mul_f32_e32 v95, v35, v243
	v_fmac_f32_e32 v83, v36, v240
	v_fmac_f32_e32 v95, v34, v242
	v_add_f32_e32 v83, v83, v95
	v_add_f32_e32 v1, v1, v83
	v_mov_b32_e32 v83, 0
	s_nop 0
	s_nop 0
	v_add_f32_dpp v1, v1, v1 row_shr:1 row_mask:0xf bank_mask:0xf bound_ctrl:1
	s_nop 0
	s_waitcnt lgkmcnt(10)
	v_mul_f32_e32 v95, v59, v251
	ds_read_b128 v[240:243], v88 offset:36864
	v_add_f32_dpp v1, v1, v1 row_shr:2 row_mask:0xf bank_mask:0xf bound_ctrl:1
	v_fmac_f32_e32 v95, v58, v250
	s_nop 0
	v_add_f32_dpp v1, v1, v1 row_shr:4 row_mask:0xf bank_mask:0xf bound_ctrl:1
	s_nop 1
	v_add_f32_dpp v1, v1, v1 row_shr:8 row_mask:0xf bank_mask:0xf bound_ctrl:1
	s_nop 1
	v_mov_b32_dpp v83, v1 row_bcast:15 row_mask:0xa bank_mask:0xf
	v_add_f32_e32 v1, v1, v83
	v_mov_b32_e32 v83, 0
	s_nop 1
	v_mov_b32_dpp v83, v1 row_bcast:31 row_mask:0xc bank_mask:0xf
	v_add_f32_e32 v1, v1, v83
	v_mul_f32_e32 v83, v63, v247
	v_readlane_b32 s39, v1, 63
	v_mul_f32_e32 v1, v65, v245
	v_fmac_f32_e32 v1, v64, v244
	v_fmac_f32_e32 v83, v62, v246
	ds_read_b128 v[244:247], v88 offset:37888
	v_add_f32_e32 v1, v1, v83
	v_mul_f32_e32 v83, v61, v249
	v_fmac_f32_e32 v83, v60, v248
	v_add_f32_e32 v1, 0, v1
	v_add_f32_e32 v83, v83, v95
	v_add_f32_e32 v1, v1, v83
	s_waitcnt lgkmcnt(11)
	v_mul_f32_e32 v83, v57, v197
	ds_read_b128 v[248:251], v88 offset:38912
	v_mul_f32_e32 v95, v55, v199
	v_fmac_f32_e32 v83, v56, v196
	v_fmac_f32_e32 v95, v54, v198
	v_add_f32_e32 v83, v83, v95
	v_add_f32_e32 v1, v1, v83
	s_waitcnt lgkmcnt(11)
	v_mul_f32_e32 v83, v53, v201
	ds_read_b128 v[196:199], v88 offset:39936
	v_mul_f32_e32 v95, v51, v203
	v_fmac_f32_e32 v83, v52, v200
	v_fmac_f32_e32 v95, v50, v202
	v_add_f32_e32 v83, v83, v95
	v_add_f32_e32 v1, v1, v83
	s_waitcnt lgkmcnt(11)
	v_mul_f32_e32 v83, v49, v205
	ds_read_b128 v[200:203], v88 offset:40960
	v_mul_f32_e32 v95, v47, v207
	v_fmac_f32_e32 v83, v48, v204
	v_fmac_f32_e32 v95, v46, v206
	v_add_f32_e32 v83, v83, v95
	v_add_f32_e32 v1, v1, v83
	s_waitcnt lgkmcnt(11)
	v_mul_f32_e32 v83, v45, v209
	ds_read_b128 v[204:207], v88 offset:41984
	v_mul_f32_e32 v95, v43, v211
	v_fmac_f32_e32 v83, v44, v208
	v_fmac_f32_e32 v95, v42, v210
	v_add_f32_e32 v83, v83, v95
	v_add_f32_e32 v1, v1, v83
	s_waitcnt lgkmcnt(11)
	v_mul_f32_e32 v83, v41, v213
	ds_read_b128 v[208:211], v88 offset:43008
	v_mul_f32_e32 v95, v39, v215
	v_fmac_f32_e32 v83, v40, v212
	v_fmac_f32_e32 v95, v38, v214
	v_add_f32_e32 v83, v83, v95
	v_add_f32_e32 v1, v1, v83
	s_waitcnt lgkmcnt(11)
	v_mul_f32_e32 v83, v37, v217
	ds_read_b128 v[212:215], v88 offset:44032
	v_mul_f32_e32 v95, v35, v219
	v_fmac_f32_e32 v83, v36, v216
	v_fmac_f32_e32 v95, v34, v218
	v_add_f32_e32 v83, v83, v95
	v_add_f32_e32 v1, v1, v83
	v_mov_b32_e32 v83, 0
	s_nop 0
	s_nop 0
	v_add_f32_dpp v1, v1, v1 row_shr:1 row_mask:0xf bank_mask:0xf bound_ctrl:1
	s_nop 0
	s_waitcnt lgkmcnt(10)
	v_mul_f32_e32 v95, v59, v227
	ds_read_b128 v[216:219], v88 offset:45056
	v_add_f32_dpp v1, v1, v1 row_shr:2 row_mask:0xf bank_mask:0xf bound_ctrl:1
	v_fmac_f32_e32 v95, v58, v226
	s_nop 0
	v_add_f32_dpp v1, v1, v1 row_shr:4 row_mask:0xf bank_mask:0xf bound_ctrl:1
	s_nop 1
	v_add_f32_dpp v1, v1, v1 row_shr:8 row_mask:0xf bank_mask:0xf bound_ctrl:1
	s_nop 1
	v_mov_b32_dpp v83, v1 row_bcast:15 row_mask:0xa bank_mask:0xf
	v_add_f32_e32 v1, v1, v83
	v_mov_b32_e32 v83, 0
	s_nop 1
	v_mov_b32_dpp v83, v1 row_bcast:31 row_mask:0xc bank_mask:0xf
	v_add_f32_e32 v1, v1, v83
	v_mul_f32_e32 v83, v63, v223
	v_readlane_b32 s60, v1, 63
	v_mul_f32_e32 v1, v65, v221
	v_fmac_f32_e32 v1, v64, v220
	v_fmac_f32_e32 v83, v62, v222
	ds_read_b128 v[220:223], v88 offset:46080
	v_add_f32_e32 v1, v1, v83
	v_mul_f32_e32 v83, v61, v225
	v_fmac_f32_e32 v83, v60, v224
	v_add_f32_e32 v1, 0, v1
	v_add_f32_e32 v83, v83, v95
	v_add_f32_e32 v1, v1, v83
	s_waitcnt lgkmcnt(11)
	v_mul_f32_e32 v83, v57, v229
	ds_read_b128 v[224:227], v88 offset:47104
	v_mul_f32_e32 v95, v55, v231
	v_fmac_f32_e32 v83, v56, v228
	v_fmac_f32_e32 v95, v54, v230
	v_add_f32_e32 v83, v83, v95
	v_add_f32_e32 v1, v1, v83
	s_waitcnt lgkmcnt(11)
	v_mul_f32_e32 v83, v53, v233
	ds_read_b128 v[228:231], v88 offset:48128
	v_mul_f32_e32 v95, v51, v235
	v_fmac_f32_e32 v83, v52, v232
	v_fmac_f32_e32 v95, v50, v234
	v_add_f32_e32 v83, v83, v95
	v_add_f32_e32 v1, v1, v83
	s_waitcnt lgkmcnt(11)
; #define LAS __attribute__((address_space(3)))
; __device__ __forceinline__ float wave_sum(float v) { return lane63(scan64<false>(v)); }
; template <int YMODE, int EXTRA, bool NORM_OUT, bool XN8  , bool XIN_BF = false  , bool XOUT_BF = false  > ...
;     ...
;                 if (EXTRA) {
;                     float d8[8];
; #pragma unroll
;                     for (int e = 0; e < 8; ++e) { float s = 0.f;
; #pragma unroll
;                         for (int j = 0; j < 8; ++j) { const f32x4 w = *(const LAS f32x4*)(we + e * D + 256 * j + 4 * F.lane); s += (x[j][0] * w[0] + x[j][1] * w[1]) + (x[j][2] * w[2] + x[j][3] * w[3]); }
;                         d8[e] = wave_sum(s); asm volatile("" ::: "memory"); }
	v_mul_f32_e32 v83, v49, v241
	ds_read_b128 v[232:235], v88 offset:49152
	v_mul_f32_e32 v95, v47, v243
	v_fmac_f32_e32 v83, v48, v240
	v_fmac_f32_e32 v95, v46, v242
	v_add_f32_e32 v83, v83, v95
	v_add_f32_e32 v1, v1, v83
	s_waitcnt lgkmcnt(11)
	v_mul_f32_e32 v83, v45, v245
	ds_read_b128 v[240:243], v88 offset:50176
	v_mul_f32_e32 v95, v43, v247
	v_fmac_f32_e32 v83, v44, v244
	v_fmac_f32_e32 v95, v42, v246
	v_add_f32_e32 v83, v83, v95
	v_add_f32_e32 v1, v1, v83
	s_waitcnt lgkmcnt(11)
	v_mul_f32_e32 v83, v41, v249
	ds_read_b128 v[244:247], v88 offset:51200
	v_mul_f32_e32 v95, v39, v251
	v_fmac_f32_e32 v83, v40, v248
	v_fmac_f32_e32 v95, v38, v250
	v_add_f32_e32 v83, v83, v95
	v_add_f32_e32 v1, v1, v83
	s_waitcnt lgkmcnt(11)
	v_mul_f32_e32 v83, v37, v197
	ds_read_b128 v[248:251], v88 offset:52224
	v_mul_f32_e32 v95, v35, v199
	v_fmac_f32_e32 v83, v36, v196
	v_fmac_f32_e32 v95, v34, v198
	v_add_f32_e32 v83, v83, v95
	v_add_f32_e32 v1, v1, v83
	v_mov_b32_e32 v83, 0
	s_nop 0
	s_nop 0
	v_add_f32_dpp v1, v1, v1 row_shr:1 row_mask:0xf bank_mask:0xf bound_ctrl:1
	s_nop 0
	s_waitcnt lgkmcnt(10)
	v_mul_f32_e32 v95, v59, v207
	ds_read_b128 v[196:199], v88 offset:53248
	v_add_f32_dpp v1, v1, v1 row_shr:2 row_mask:0xf bank_mask:0xf bound_ctrl:1
	v_fmac_f32_e32 v95, v58, v206
	s_nop 0
	v_add_f32_dpp v1, v1, v1 row_shr:4 row_mask:0xf bank_mask:0xf bound_ctrl:1
	s_nop 1
	v_add_f32_dpp v1, v1, v1 row_shr:8 row_mask:0xf bank_mask:0xf bound_ctrl:1
	s_nop 1
	v_mov_b32_dpp v83, v1 row_bcast:15 row_mask:0xa bank_mask:0xf
	v_add_f32_e32 v1, v1, v83
	v_mov_b32_e32 v83, 0
	s_nop 1
	v_mov_b32_dpp v83, v1 row_bcast:31 row_mask:0xc bank_mask:0xf
	v_add_f32_e32 v1, v1, v83
	v_mul_f32_e32 v83, v63, v203
	v_readlane_b32 s61, v1, 63
	v_mul_f32_e32 v1, v65, v201
	v_fmac_f32_e32 v1, v64, v200
	v_fmac_f32_e32 v83, v62, v202
	ds_read_b128 v[200:203], v88 offset:54272
	v_add_f32_e32 v1, v1, v83
	v_mul_f32_e32 v83, v61, v205
	v_fmac_f32_e32 v83, v60, v204
	v_add_f32_e32 v1, 0, v1
	v_add_f32_e32 v83, v83, v95
	v_add_f32_e32 v1, v1, v83
	s_waitcnt lgkmcnt(11)
	v_mul_f32_e32 v83, v57, v209
	ds_read_b128 v[204:207], v88 offset:55296
	v_mul_f32_e32 v95, v55, v211
	v_fmac_f32_e32 v83, v56, v208
	v_fmac_f32_e32 v95, v54, v210
	v_add_f32_e32 v83, v83, v95
	v_add_f32_e32 v1, v1, v83
	s_waitcnt lgkmcnt(11)
	v_mul_f32_e32 v83, v53, v213
	ds_read_b128 v[208:211], v88 offset:56320
	v_mul_f32_e32 v95, v51, v215
	v_fmac_f32_e32 v83, v52, v212
	v_fmac_f32_e32 v95, v50, v214
	v_add_f32_e32 v83, v83, v95
	v_add_f32_e32 v1, v1, v83
	s_waitcnt lgkmcnt(11)
	v_mul_f32_e32 v83, v49, v217
	ds_read_b128 v[212:215], v88 offset:57344
	v_mul_f32_e32 v95, v47, v219
	v_fmac_f32_e32 v83, v48, v216
	v_fmac_f32_e32 v95, v46, v218
	v_add_f32_e32 v83, v83, v95
	v_add_f32_e32 v1, v1, v83
	s_waitcnt lgkmcnt(11)
	v_mul_f32_e32 v83, v45, v221
	ds_read_b128 v[216:219], v88 offset:58368
	v_mul_f32_e32 v95, v43, v223
	v_fmac_f32_e32 v83, v44, v220
	v_fmac_f32_e32 v95, v42, v222
	v_add_f32_e32 v83, v83, v95
	v_add_f32_e32 v1, v1, v83
	s_waitcnt lgkmcnt(11)
	v_mul_f32_e32 v83, v41, v225
	ds_read_b128 v[220:223], v88 offset:59392
	v_mul_f32_e32 v95, v39, v227
	v_fmac_f32_e32 v83, v40, v224
	v_fmac_f32_e32 v95, v38, v226
	v_add_f32_e32 v83, v83, v95
	v_add_f32_e32 v1, v1, v83
	s_waitcnt lgkmcnt(11)
	v_mul_f32_e32 v83, v37, v229
	ds_read_b128 v[224:227], v88 offset:60416
	v_mul_f32_e32 v95, v35, v231
	v_fmac_f32_e32 v83, v36, v228
	v_fmac_f32_e32 v95, v34, v230
	v_add_f32_e32 v83, v83, v95
	v_add_f32_e32 v1, v1, v83
	v_mov_b32_e32 v83, 0
	s_nop 0
	s_nop 0
	v_add_f32_dpp v1, v1, v1 row_shr:1 row_mask:0xf bank_mask:0xf bound_ctrl:1
	s_nop 0
	s_waitcnt lgkmcnt(10)
	v_mul_f32_e32 v95, v59, v243
	ds_read_b128 v[228:231], v88 offset:61440
	v_add_f32_dpp v1, v1, v1 row_shr:2 row_mask:0xf bank_mask:0xf bound_ctrl:1
	v_fmac_f32_e32 v95, v58, v242
	s_nop 0
	v_add_f32_dpp v1, v1, v1 row_shr:4 row_mask:0xf bank_mask:0xf bound_ctrl:1
	s_nop 1
	v_add_f32_dpp v1, v1, v1 row_shr:8 row_mask:0xf bank_mask:0xf bound_ctrl:1
	s_nop 1
	v_mov_b32_dpp v83, v1 row_bcast:15 row_mask:0xa bank_mask:0xf
	v_add_f32_e32 v1, v1, v83
	v_mov_b32_e32 v83, 0
	s_nop 1
	v_mov_b32_dpp v83, v1 row_bcast:31 row_mask:0xc bank_mask:0xf
	v_add_f32_e32 v1, v1, v83
	v_mul_f32_e32 v83, v63, v235
	v_readlane_b32 s62, v1, 63
	v_mul_f32_e32 v1, v65, v233
	v_fmac_f32_e32 v1, v64, v232
	v_fmac_f32_e32 v83, v62, v234
	ds_read_b128 v[232:235], v88 offset:62464
	v_add_f32_e32 v1, v1, v83
	v_mul_f32_e32 v83, v61, v241
	v_fmac_f32_e32 v83, v60, v240
	v_add_f32_e32 v1, 0, v1
	v_add_f32_e32 v83, v83, v95
	v_add_f32_e32 v1, v1, v83
	s_waitcnt lgkmcnt(11)
	v_mul_f32_e32 v83, v57, v245
	ds_read_b128 v[240:243], v88 offset:63488
	v_mul_f32_e32 v95, v55, v247
	v_fmac_f32_e32 v83, v56, v244
	v_fmac_f32_e32 v95, v54, v246
	v_add_f32_e32 v83, v83, v95
	v_add_f32_e32 v1, v1, v83
	s_waitcnt lgkmcnt(11)
	v_mul_f32_e32 v83, v53, v249
	ds_read_b128 v[244:247], v88 offset:64512
	v_mul_f32_e32 v95, v51, v251
	v_fmac_f32_e32 v83, v52, v248
	v_fmac_f32_e32 v95, v50, v250
	v_add_f32_e32 v83, v83, v95
	v_add_f32_e32 v1, v1, v83
	s_waitcnt lgkmcnt(11)
; #define LAS __attribute__((address_space(3)))
; __device__ __forceinline__ float wave_sum(float v) { return lane63(scan64<false>(v)); }
; template <int YMODE, int EXTRA, bool NORM_OUT, bool XN8  , bool XIN_BF = false  , bool XOUT_BF = false  > ...
;     ...
;                 if (EXTRA) {
;                     float d8[8];
; #pragma unroll
;                     for (int e = 0; e < 8; ++e) { float s = 0.f;
; #pragma unroll
;                         for (int j = 0; j < 8; ++j) { const f32x4 w = *(const LAS f32x4*)(we + e * D + 256 * j + 4 * F.lane); s += (x[j][0] * w[0] + x[j][1] * w[1]) + (x[j][2] * w[2] + x[j][3] * w[3]); }
;                         d8[e] = wave_sum(s); asm volatile("" ::: "memory"); }
;                     if (EXTRA == 1) {
;                         float v = 0.f;
; #pragma unroll
;                         for (int e = 0; e < 8; ++e) v = (F.lane == e) ? d8[e] : v;
;                         if (F.lane < 8) { const float bb = (F.lane < 4) ? bi[F.lane] : bfg[F.lane - 4]; const float z = 15.f * tanhf((v + bb) * (1.f / 15.f));
;                             const float o = (F.lane < 4) ? z : (fminf(z, 0.f) - log1pf(expf(-fabsf(z)))); gates_out[row * 8 + F.lane] = o; }
	v_mul_f32_e32 v83, v49, v197
	v_mul_f32_e32 v95, v47, v199
	v_fmac_f32_e32 v83, v48, v196
	v_fmac_f32_e32 v95, v46, v198
	v_add_f32_e32 v83, v83, v95
	v_add_f32_e32 v1, v1, v83
	s_waitcnt lgkmcnt(10)
	v_mul_f32_e32 v83, v45, v201
	v_mul_f32_e32 v95, v43, v203
	v_fmac_f32_e32 v83, v44, v200
	v_fmac_f32_e32 v95, v42, v202
	v_add_f32_e32 v83, v83, v95
	v_add_f32_e32 v1, v1, v83
	s_waitcnt lgkmcnt(9)
	v_mul_f32_e32 v83, v41, v205
	v_mul_f32_e32 v95, v39, v207
	v_fmac_f32_e32 v83, v40, v204
	v_fmac_f32_e32 v95, v38, v206
	v_add_f32_e32 v83, v83, v95
	v_add_f32_e32 v1, v1, v83
	s_waitcnt lgkmcnt(8)
	v_mul_f32_e32 v83, v37, v209
	v_mul_f32_e32 v95, v35, v211
	v_fmac_f32_e32 v83, v36, v208
	v_fmac_f32_e32 v95, v34, v210
	v_add_f32_e32 v83, v83, v95
	v_add_f32_e32 v1, v1, v83
	v_mov_b32_e32 v83, 0
	s_nop 0
	s_nop 0
	v_add_f32_dpp v1, v1, v1 row_shr:1 row_mask:0xf bank_mask:0xf bound_ctrl:1
	s_nop 0
	s_waitcnt lgkmcnt(7)
	v_mul_f32_e32 v63, v63, v215
	v_add_f32_dpp v1, v1, v1 row_shr:2 row_mask:0xf bank_mask:0xf bound_ctrl:1
	v_fmac_f32_e32 v63, v62, v214
	s_waitcnt lgkmcnt(6)
	v_mul_f32_e32 v59, v59, v219
	v_add_f32_dpp v1, v1, v1 row_shr:4 row_mask:0xf bank_mask:0xf bound_ctrl:1
	v_fmac_f32_e32 v59, v58, v218
	s_nop 0
	v_add_f32_dpp v1, v1, v1 row_shr:8 row_mask:0xf bank_mask:0xf bound_ctrl:1
	s_nop 1
	v_mov_b32_dpp v83, v1 row_bcast:15 row_mask:0xa bank_mask:0xf
	v_add_f32_e32 v1, v1, v83
	v_mov_b32_e32 v83, 0
	s_nop 1
	v_mov_b32_dpp v83, v1 row_bcast:31 row_mask:0xc bank_mask:0xf
	v_add_f32_e32 v1, v1, v83
	s_nop 0
	v_readlane_b32 s63, v1, 63
	v_mul_f32_e32 v1, v65, v213
	v_fmac_f32_e32 v1, v64, v212
	v_mul_f32_e32 v64, v61, v217
	v_add_f32_e32 v1, v1, v63
	v_fmac_f32_e32 v64, v60, v216
	v_add_f32_e32 v1, 0, v1
	v_add_f32_e32 v58, v64, v59
	v_add_f32_e32 v1, v1, v58
	s_waitcnt lgkmcnt(5)
	v_mul_f32_e32 v57, v57, v221
	v_mul_f32_e32 v55, v55, v223
	v_fmac_f32_e32 v57, v56, v220
	v_fmac_f32_e32 v55, v54, v222
	v_add_f32_e32 v54, v57, v55
	s_waitcnt lgkmcnt(4)
	v_mul_f32_e32 v56, v53, v225
	v_add_f32_e32 v1, v1, v54
	v_fmac_f32_e32 v56, v52, v224
	v_mul_f32_e32 v51, v51, v227
	v_fmac_f32_e32 v51, v50, v226
	v_add_f32_e32 v50, v56, v51
	v_add_f32_e32 v1, v1, v50
	s_waitcnt lgkmcnt(3)
	v_mul_f32_e32 v49, v49, v229
	v_mul_f32_e32 v47, v47, v231
	v_fmac_f32_e32 v49, v48, v228
	v_fmac_f32_e32 v47, v46, v230
	v_add_f32_e32 v46, v49, v47
	s_waitcnt lgkmcnt(2)
	v_mul_f32_e32 v48, v45, v233
	v_mul_f32_e32 v43, v43, v235
	v_add_f32_e32 v1, v1, v46
	v_fmac_f32_e32 v48, v44, v232
	v_fmac_f32_e32 v43, v42, v234
	v_add_f32_e32 v42, v48, v43
	v_add_f32_e32 v1, v1, v42
	s_waitcnt lgkmcnt(1)
	v_mul_f32_e32 v41, v41, v241
	v_mul_f32_e32 v39, v39, v243
	v_fmac_f32_e32 v41, v40, v240
	v_fmac_f32_e32 v39, v38, v242
	s_waitcnt lgkmcnt(0)
	v_mul_f32_e32 v37, v37, v245
	v_mul_f32_e32 v35, v35, v247
	v_add_f32_e32 v38, v41, v39
	v_fmac_f32_e32 v37, v36, v244
	v_fmac_f32_e32 v35, v34, v246
	v_add_f32_e32 v1, v1, v38
	v_add_f32_e32 v34, v37, v35
	v_add_f32_e32 v1, v1, v34
	v_mov_b32_e32 v34, 0
	s_nop 0
	v_add_f32_dpp v1, v1, v1 row_shr:1 row_mask:0xf bank_mask:0xf bound_ctrl:1
	s_nop 1
	v_add_f32_dpp v1, v1, v1 row_shr:2 row_mask:0xf bank_mask:0xf bound_ctrl:1
	s_nop 1
	v_add_f32_dpp v1, v1, v1 row_shr:4 row_mask:0xf bank_mask:0xf bound_ctrl:1
	s_nop 1
	v_add_f32_dpp v1, v1, v1 row_shr:8 row_mask:0xf bank_mask:0xf bound_ctrl:1
	s_nop 1
	v_mov_b32_dpp v34, v1 row_bcast:15 row_mask:0xa bank_mask:0xf
	v_add_f32_e32 v1, v1, v34
	v_mov_b32_e32 v34, 0
	s_nop 1
	v_mov_b32_dpp v34, v1 row_bcast:31 row_mask:0xc bank_mask:0xf
	v_add_f32_e32 v1, v1, v34
	s_nop 0
	v_readlane_b32 s64, v1, 63
	s_and_saveexec_b64 s[36:37], s[8:9]
	s_cbranch_execz .LBB0_107
	global_load_dword v1, v[76:77], off
	v_mov_b32_e32 v34, s34
	v_cndmask_b32_e64 v34, 0, v34, s[6:7]
	v_mov_b32_e32 v35, s38
	v_cndmask_b32_e64 v34, v34, v35, s[22:23]
	v_mov_b32_e32 v35, s39
	v_cndmask_b32_e64 v34, v34, v35, s[20:21]
	v_mov_b32_e32 v35, s60
	v_cndmask_b32_e64 v34, v34, v35, s[18:19]
	v_mov_b32_e32 v35, s61
	v_cndmask_b32_e64 v34, v34, v35, s[16:17]
	v_mov_b32_e32 v35, s62
	v_cndmask_b32_e64 v34, v34, v35, s[14:15]
	v_mov_b32_e32 v35, s63
	v_cndmask_b32_e64 v34, v34, v35, s[12:13]
	v_mov_b32_e32 v35, s64
	v_cndmask_b32_e64 v34, v34, v35, s[10:11]
	s_waitcnt vmcnt(0) lgkmcnt(0)
	v_add_f32_e32 v1, v34, v1
	v_mul_f32_e32 v1, 0x3d888889, v1
	v_cmp_nlt_f32_e64 s[38:39], |v1|, s43
	s_and_saveexec_b64 s[60:61], s[38:39]
	s_xor_b64 s[38:39], exec, s[60:61]
	s_cbranch_execz .LBB0_115
	v_add_f32_e64 v34, |v1|, |v1|
	v_mul_f32_e32 v35, 0x3fb8aa3b, v34
	v_rndne_f32_e32 v36, v35
	v_sub_f32_e32 v37, v35, v36
	v_fma_f32 v35, v34, s44, -v35
	v_fmac_f32_e32 v35, 0x32a5705f, v34
	v_add_f32_e32 v35, v37, v35
	v_cvt_i32_f32_e32 v36, v36
	v_exp_f32_e32 v35, v35
	v_cmp_ngt_f32_e32 vcc, s45, v34
	v_ldexp_f32 v35, v35, v36
	s_nop 0
	v_cndmask_b32_e32 v35, 0, v35, vcc
	v_cmp_nlt_f32_e32 vcc, s46, v34
	s_nop 1
	v_cndmask_b32_e32 v34, v94, v35, vcc
	v_add_f32_e32 v34, 1.0, v34
	v_rcp_f32_e32 v34, v34
	s_nop 0
	v_fma_f32 v34, v34, -2.0, 1.0

; #define LAS __attribute__((address_space(3)))
; __device__ __forceinline__ unsigned cvtpk(float lo, float hi) { f32x2 v = {lo, hi}; bf16x2_t b = __builtin_convertvector(v, bf16x2_t); return __builtin_bit_cast(unsigned, b); }
; __device__ __forceinline__ float wave_sum(float v) { return lane63(scan64<false>(v)); }
; __device__ __forceinline__ float wave_max(float v) { return lane63(scan64<true>(v)); }
; template <int YMODE, int EXTRA, bool NORM_OUT, bool XN8  , bool XIN_BF = false  , bool XOUT_BF = false  > ...
;     ...
;                 if (XN8) {
;                     float am = 0.f;
; #pragma unroll
;                     for (int j = 0; j < 8; ++j) am = fmaxf(fmaxf(am, fmaxf(fabsf(x[j][0]), fabsf(x[j][1]))), fmaxf(fabsf(x[j][2]), fabsf(x[j][3])));
;                     am = wave_max(am);
;                     const float inv = am > 0.f ? 127.f / am : 0.f;
;                     if (F.lane == 0) { rowmax[row] = am; if (EXTRA == 2) route[384 + rl] = am; }
; #pragma unroll
;                     for (int j = 0; j < 8; ++j) *(unsigned*)((unsigned char*)XN + row * D + 256 * j + 4 * F.lane) = pack_i8x4(x[j][0] * inv, x[j][1] * inv, x[j][2] * inv, x[j][3] * inv);
;                 } else {
; #pragma unroll
;                     for (int j = 0; j < 8; ++j) { u32x2 w; w.x = cvtpk(x[j][0], x[j][1]); w.y = cvtpk(x[j][2], x[j][3]); *(u32x2*)(XN + row * D + 256 * j + 4 * F.lane) = w; }
;                 }
;                 if (EXTRA) {
;                     float d8[8];
; #pragma unroll
;                     for (int e = 0; e < 8; ++e) { float s = 0.f;
; #pragma unroll
;                         for (int j = 0; j < 8; ++j) { const f32x4 w = *(const LAS f32x4*)(we + e * D + 256 * j + 4 * F.lane); s += (x[j][0] * w[0] + x[j][1] * w[1]) + (x[j][2] * w[2] + x[j][3] * w[3]); }
;                         d8[e] = wave_sum(s); asm volatile("" ::: "memory"); }
.LBB0_1311:
	s_or_b64 exec, exec, s[26:27]
	ds_read_b128 v[196:199], v105
	ds_read_b128 v[200:203], v105 offset:1024
	ds_read_b128 v[204:207], v105 offset:2048
	ds_read_b128 v[208:211], v105 offset:3072
	ds_read_b128 v[212:215], v105 offset:4096
	ds_read_b128 v[216:219], v105 offset:5120
	ds_read_b128 v[220:223], v105 offset:6144
	ds_read_b128 v[224:227], v105 offset:7168
	ds_read_b128 v[228:231], v105 offset:8192
	ds_read_b128 v[232:235], v105 offset:9216
	ds_read_b128 v[240:243], v105 offset:10240
	ds_read_b128 v[244:247], v105 offset:11264
	v_div_scale_f32 v1, s[26:27], s34, s34, v110
	v_rcp_f32_e32 v25, v1
	v_mov_b32_e32 v90, s34
	s_mov_b32 s26, 0x42fe0000
	v_div_scale_f32 v90, vcc, s26, v90, s26
	v_fma_f32 v91, -v1, v25, 1.0
	v_fmac_f32_e32 v25, v91, v25
	v_mul_f32_e32 v91, v90, v25
	v_fma_f32 v92, -v1, v91, v90
	v_fmac_f32_e32 v91, v92, v25
	v_fma_f32 v1, -v1, v91, v90
	v_div_fmas_f32 v1, v1, v25, v91
	v_div_fixup_f32 v1, v1, s34, v110
	v_cmp_gt_f32_e64 vcc, s34, 0
	s_lshl_b64 s[26:27], s[36:37], 11
	v_lshl_add_u64 v[94:95], v[22:23], 0, s[26:27]
	v_cndmask_b32_e32 v1, 0, v1, vcc
	v_mul_f32_e32 v90, v85, v1
	v_mul_f32_e32 v25, v84, v1
	v_mul_f32_e32 v91, v72, v1
	v_mul_f32_e32 v92, v73, v1
	v_med3_f32 v90, v90, s42, v110
	v_med3_f32 v25, v25, s42, v110
	v_rndne_f32_e32 v90, v90
	v_med3_f32 v91, v91, s42, v110
	v_med3_f32 v92, v92, s42, v110
	v_rndne_f32_e32 v25, v25
	v_cvt_i32_f32_e32 v90, v90
	v_rndne_f32_e32 v91, v91
	v_rndne_f32_e32 v92, v92
	v_cvt_i32_f32_e32 v25, v25
	v_cvt_i32_f32_sdwa v91, v91 dst_sel:WORD_1 dst_unused:UNUSED_PAD src0_sel:DWORD
	v_cvt_i32_f32_e32 v92, v92
	v_lshlrev_b32_e32 v90, 8, v90
	v_and_b32_e32 v90, 0xff00, v90
	v_and_b32_e32 v91, 0xff0000, v91
	v_perm_b32 v25, v92, v25, s43
	v_or3_b32 v25, v25, v90, v91
	v_mul_f32_e32 v90, v89, v1
	global_store_dword v[94:95], v25, off
	v_mul_f32_e32 v25, v88, v1
	v_mul_f32_e32 v91, v62, v1
	v_mul_f32_e32 v92, v63, v1
	v_med3_f32 v90, v90, s42, v110
	v_med3_f32 v25, v25, s42, v110
	v_rndne_f32_e32 v90, v90
	v_med3_f32 v91, v91, s42, v110
	v_med3_f32 v92, v92, s42, v110
	v_rndne_f32_e32 v25, v25
	v_cvt_i32_f32_e32 v90, v90
	v_rndne_f32_e32 v91, v91
	v_rndne_f32_e32 v92, v92
	v_cvt_i32_f32_e32 v25, v25
	v_cvt_i32_f32_sdwa v91, v91 dst_sel:WORD_1 dst_unused:UNUSED_PAD src0_sel:DWORD
	v_cvt_i32_f32_e32 v92, v92
	v_lshlrev_b32_e32 v90, 8, v90
	v_and_b32_e32 v90, 0xff00, v90
	v_and_b32_e32 v91, 0xff0000, v91
	v_perm_b32 v25, v92, v25, s43
	v_or3_b32 v25, v25, v90, v91
	v_mul_f32_e32 v90, v81, v1
	global_store_dword v[94:95], v25, off offset:256
	v_mul_f32_e32 v25, v80, v1
	v_mul_f32_e32 v91, v70, v1
	v_mul_f32_e32 v92, v71, v1
	v_med3_f32 v90, v90, s42, v110
	v_med3_f32 v25, v25, s42, v110
	v_rndne_f32_e32 v90, v90
	v_med3_f32 v91, v91, s42, v110
	v_med3_f32 v92, v92, s42, v110
	v_rndne_f32_e32 v25, v25
	v_cvt_i32_f32_e32 v90, v90
	v_rndne_f32_e32 v91, v91
	v_rndne_f32_e32 v92, v92
	v_cvt_i32_f32_e32 v25, v25
	v_cvt_i32_f32_sdwa v91, v91 dst_sel:WORD_1 dst_unused:UNUSED_PAD src0_sel:DWORD
	v_cvt_i32_f32_e32 v92, v92
	v_lshlrev_b32_e32 v90, 8, v90
	v_and_b32_e32 v90, 0xff00, v90
	v_and_b32_e32 v91, 0xff0000, v91
	v_perm_b32 v25, v92, v25, s43
	v_or3_b32 v25, v25, v90, v91
	v_mul_f32_e32 v90, v87, v1
	global_store_dword v[94:95], v25, off offset:512
	v_mul_f32_e32 v25, v86, v1
	v_mul_f32_e32 v91, v60, v1
	v_mul_f32_e32 v92, v61, v1
	v_med3_f32 v90, v90, s42, v110
	v_med3_f32 v25, v25, s42, v110
	v_rndne_f32_e32 v90, v90
	v_med3_f32 v91, v91, s42, v110
	v_med3_f32 v92, v92, s42, v110
	v_rndne_f32_e32 v25, v25
	v_cvt_i32_f32_e32 v90, v90
	v_rndne_f32_e32 v91, v91
	v_rndne_f32_e32 v92, v92
	v_cvt_i32_f32_e32 v25, v25
	v_cvt_i32_f32_sdwa v91, v91 dst_sel:WORD_1 dst_unused:UNUSED_PAD src0_sel:DWORD
	v_cvt_i32_f32_e32 v92, v92
	v_lshlrev_b32_e32 v90, 8, v90
	v_and_b32_e32 v90, 0xff00, v90
	v_and_b32_e32 v91, 0xff0000, v91
	v_perm_b32 v25, v92, v25, s43
	v_or3_b32 v25, v25, v90, v91
	v_mul_f32_e32 v90, v77, v1
	global_store_dword v[94:95], v25, off offset:768
	v_mul_f32_e32 v25, v76, v1
	v_mul_f32_e32 v91, v68, v1
	v_mul_f32_e32 v92, v69, v1
	v_med3_f32 v90, v90, s42, v110
	v_med3_f32 v25, v25, s42, v110
	v_rndne_f32_e32 v90, v90
	v_med3_f32 v91, v91, s42, v110
	v_med3_f32 v92, v92, s42, v110
	v_rndne_f32_e32 v25, v25
	v_cvt_i32_f32_e32 v90, v90
	v_rndne_f32_e32 v91, v91
	v_rndne_f32_e32 v92, v92
	v_cvt_i32_f32_e32 v25, v25
	v_cvt_i32_f32_sdwa v91, v91 dst_sel:WORD_1 dst_unused:UNUSED_PAD src0_sel:DWORD
	v_cvt_i32_f32_e32 v92, v92
	v_lshlrev_b32_e32 v90, 8, v90
	v_and_b32_e32 v90, 0xff00, v90
	v_and_b32_e32 v91, 0xff0000, v91
	v_perm_b32 v25, v92, v25, s43
	v_or3_b32 v25, v25, v90, v91
	v_mul_f32_e32 v90, v83, v1
	global_store_dword v[94:95], v25, off offset:1024
	v_mul_f32_e32 v25, v82, v1
	v_mul_f32_e32 v91, v58, v1
	v_mul_f32_e32 v92, v59, v1
	v_med3_f32 v90, v90, s42, v110
	v_med3_f32 v25, v25, s42, v110
	v_rndne_f32_e32 v90, v90
	v_med3_f32 v91, v91, s42, v110
	v_med3_f32 v92, v92, s42, v110
	v_rndne_f32_e32 v25, v25
	v_cvt_i32_f32_e32 v90, v90
	v_rndne_f32_e32 v91, v91
	v_rndne_f32_e32 v92, v92
	v_cvt_i32_f32_e32 v25, v25
	v_cvt_i32_f32_sdwa v91, v91 dst_sel:WORD_1 dst_unused:UNUSED_PAD src0_sel:DWORD
	v_cvt_i32_f32_e32 v92, v92
	v_lshlrev_b32_e32 v90, 8, v90
	v_and_b32_e32 v90, 0xff00, v90
	v_and_b32_e32 v91, 0xff0000, v91
	v_perm_b32 v25, v92, v25, s43
	v_or3_b32 v25, v25, v90, v91
	v_mul_f32_e32 v90, v75, v1
	global_store_dword v[94:95], v25, off offset:1280
	v_mul_f32_e32 v25, v74, v1
	v_mul_f32_e32 v91, v64, v1
	v_mul_f32_e32 v92, v65, v1
	v_med3_f32 v90, v90, s42, v110
	v_med3_f32 v25, v25, s42, v110
	v_rndne_f32_e32 v90, v90
	v_med3_f32 v91, v91, s42, v110
	v_med3_f32 v92, v92, s42, v110
	v_rndne_f32_e32 v25, v25
	v_cvt_i32_f32_e32 v90, v90
	v_rndne_f32_e32 v91, v91
	v_rndne_f32_e32 v92, v92
	v_cvt_i32_f32_e32 v25, v25
	v_cvt_i32_f32_sdwa v91, v91 dst_sel:WORD_1 dst_unused:UNUSED_PAD src0_sel:DWORD
	v_cvt_i32_f32_e32 v92, v92
	v_lshlrev_b32_e32 v90, 8, v90
	v_and_b32_e32 v90, 0xff00, v90
	v_and_b32_e32 v91, 0xff0000, v91
	v_perm_b32 v25, v92, v25, s43
	v_or3_b32 v25, v25, v90, v91
	v_mul_f32_e32 v90, v79, v1
	global_store_dword v[94:95], v25, off offset:1536
	v_mul_f32_e32 v25, v78, v1
	v_mul_f32_e32 v91, v66, v1
	v_mul_f32_e32 v1, v67, v1
	v_med3_f32 v90, v90, s42, v110
	v_med3_f32 v25, v25, s42, v110
	v_rndne_f32_e32 v90, v90
	v_med3_f32 v91, v91, s42, v110
	v_med3_f32 v1, v1, s42, v110
	v_rndne_f32_e32 v25, v25
	v_cvt_i32_f32_e32 v90, v90
	v_rndne_f32_e32 v91, v91
	v_rndne_f32_e32 v1, v1
	v_cvt_i32_f32_e32 v25, v25
	v_cvt_i32_f32_sdwa v91, v91 dst_sel:WORD_1 dst_unused:UNUSED_PAD src0_sel:DWORD
	v_cvt_i32_f32_e32 v1, v1
	v_lshlrev_b32_e32 v90, 8, v90
	v_and_b32_e32 v96, 0xff00, v90
	v_and_b32_e32 v97, 0xff0000, v91
	s_nop 0
	v_perm_b32 v1, v1, v25, s43
	v_or3_b32 v1, v1, v96, v97
	global_store_dword v[94:95], v1, off offset:1792
	s_nop 0
	s_waitcnt lgkmcnt(12)
; #define LAS __attribute__((address_space(3)))
; __device__ __forceinline__ float wave_sum(float v) { return lane63(scan64<false>(v)); }
; template <int YMODE, int EXTRA, bool NORM_OUT, bool XN8  , bool XIN_BF = false  , bool XOUT_BF = false  > ...
;     ...
;                 if (EXTRA) {
;                     float d8[8];
; #pragma unroll
;                     for (int e = 0; e < 8; ++e) { float s = 0.f;
; #pragma unroll
;                         for (int j = 0; j < 8; ++j) { const f32x4 w = *(const LAS f32x4*)(we + e * D + 256 * j + 4 * F.lane); s += (x[j][0] * w[0] + x[j][1] * w[1]) + (x[j][2] * w[2] + x[j][3] * w[3]); }
;                         d8[e] = wave_sum(s); asm volatile("" ::: "memory"); }
	s_waitcnt lgkmcnt(11)
	v_mul_f32_e32 v1, v85, v197
	ds_read_b128 v[248:251], v105 offset:12288
	v_mul_f32_e32 v25, v73, v199
	v_fmac_f32_e32 v1, v84, v196
	v_fmac_f32_e32 v25, v72, v198
	v_add_f32_e32 v1, v1, v25
	s_waitcnt lgkmcnt(11)
	v_mul_f32_e32 v25, v89, v201
	ds_read_b128 v[196:199], v105 offset:13312
	v_fmac_f32_e32 v25, v88, v200
	v_mul_f32_e32 v94, v63, v203
	v_fmac_f32_e32 v94, v62, v202
	v_add_f32_e32 v1, 0, v1
	v_add_f32_e32 v25, v25, v94
	v_add_f32_e32 v1, v1, v25
	s_waitcnt lgkmcnt(11)
	v_mul_f32_e32 v25, v81, v205
	ds_read_b128 v[200:203], v105 offset:14336
	v_fmac_f32_e32 v25, v80, v204
	v_mul_f32_e32 v90, v71, v207
	v_fmac_f32_e32 v90, v70, v206
	v_add_f32_e32 v25, v25, v90
	v_add_f32_e32 v1, v1, v25
	s_waitcnt lgkmcnt(11)
	v_mul_f32_e32 v25, v87, v209
	ds_read_b128 v[204:207], v105 offset:15360
	v_fmac_f32_e32 v25, v86, v208
	v_mul_f32_e32 v94, v61, v211
	v_fmac_f32_e32 v94, v60, v210
	v_add_f32_e32 v25, v25, v94
	v_add_f32_e32 v1, v1, v25
	s_waitcnt lgkmcnt(11)
	v_mul_f32_e32 v25, v77, v213
	ds_read_b128 v[208:211], v105 offset:16384
	v_fmac_f32_e32 v25, v76, v212
	v_mul_f32_e32 v90, v69, v215
	v_fmac_f32_e32 v90, v68, v214
	v_add_f32_e32 v25, v25, v90
	v_add_f32_e32 v1, v1, v25
	s_waitcnt lgkmcnt(11)
	v_mul_f32_e32 v25, v83, v217
	ds_read_b128 v[212:215], v105 offset:17408
	v_fmac_f32_e32 v25, v82, v216
	v_mul_f32_e32 v94, v59, v219
	v_fmac_f32_e32 v94, v58, v218
	v_add_f32_e32 v25, v25, v94
	v_add_f32_e32 v1, v1, v25
	s_waitcnt lgkmcnt(11)
	v_mul_f32_e32 v25, v75, v221
	ds_read_b128 v[216:219], v105 offset:18432
	v_fmac_f32_e32 v25, v74, v220
	v_mul_f32_e32 v90, v65, v223
	v_fmac_f32_e32 v90, v64, v222
	v_add_f32_e32 v25, v25, v90
	v_add_f32_e32 v1, v1, v25
	s_waitcnt lgkmcnt(11)
	v_mul_f32_e32 v25, v79, v225
	ds_read_b128 v[220:223], v105 offset:19456
	v_mul_f32_e32 v90, v67, v227
	v_fmac_f32_e32 v25, v78, v224
	v_fmac_f32_e32 v90, v66, v226
	v_add_f32_e32 v25, v25, v90
	v_add_f32_e32 v1, v1, v25
	v_mov_b32_e32 v25, 0
	s_nop 0
	s_nop 0
	v_add_f32_dpp v1, v1, v1 row_shr:1 row_mask:0xf bank_mask:0xf bound_ctrl:1
	s_nop 1
	v_add_f32_dpp v1, v1, v1 row_shr:2 row_mask:0xf bank_mask:0xf bound_ctrl:1
	s_nop 1
	v_add_f32_dpp v1, v1, v1 row_shr:4 row_mask:0xf bank_mask:0xf bound_ctrl:1
	s_nop 1
	v_add_f32_dpp v1, v1, v1 row_shr:8 row_mask:0xf bank_mask:0xf bound_ctrl:1
	s_nop 1
	v_mov_b32_dpp v25, v1 row_bcast:15 row_mask:0xa bank_mask:0xf
	v_add_f32_e32 v1, v1, v25
	v_mov_b32_e32 v25, 0
	s_nop 1
	v_mov_b32_dpp v25, v1 row_bcast:31 row_mask:0xc bank_mask:0xf
	v_add_f32_e32 v1, v1, v25
	s_nop 0
	s_waitcnt lgkmcnt(11)
	v_mul_f32_e32 v25, v73, v231
	ds_read_b128 v[224:227], v105 offset:20480
	v_readlane_b32 s34, v1, 63
	v_mul_f32_e32 v1, v85, v229
	v_fmac_f32_e32 v1, v84, v228
	v_fmac_f32_e32 v25, v72, v230
	v_add_f32_e32 v1, v1, v25
	s_waitcnt lgkmcnt(11)
	v_mul_f32_e32 v25, v89, v233
	ds_read_b128 v[228:231], v105 offset:21504
	v_fmac_f32_e32 v25, v88, v232
	v_mul_f32_e32 v94, v63, v235
	v_fmac_f32_e32 v94, v62, v234
	v_add_f32_e32 v1, 0, v1
	v_add_f32_e32 v25, v25, v94
	v_add_f32_e32 v1, v1, v25
	s_waitcnt lgkmcnt(11)
	v_mul_f32_e32 v25, v81, v241
	ds_read_b128 v[232:235], v105 offset:22528
	v_fmac_f32_e32 v25, v80, v240
	v_mul_f32_e32 v90, v71, v243
	v_fmac_f32_e32 v90, v70, v242
	v_add_f32_e32 v25, v25, v90
	v_add_f32_e32 v1, v1, v25
	s_waitcnt lgkmcnt(11)
	v_mul_f32_e32 v25, v87, v245
	ds_read_b128 v[240:243], v105 offset:23552
	v_fmac_f32_e32 v25, v86, v244
	v_mul_f32_e32 v94, v61, v247
	v_fmac_f32_e32 v94, v60, v246
	v_add_f32_e32 v25, v25, v94
	v_add_f32_e32 v1, v1, v25
	s_waitcnt lgkmcnt(11)
	v_mul_f32_e32 v25, v77, v249
	ds_read_b128 v[244:247], v105 offset:24576
	v_fmac_f32_e32 v25, v76, v248
	v_mul_f32_e32 v90, v69, v251
	v_fmac_f32_e32 v90, v68, v250
	v_add_f32_e32 v25, v25, v90
	v_add_f32_e32 v1, v1, v25
	s_waitcnt lgkmcnt(11)
	v_mul_f32_e32 v25, v83, v197
	ds_read_b128 v[248:251], v105 offset:25600
	v_fmac_f32_e32 v25, v82, v196
	v_mul_f32_e32 v94, v59, v199
	v_fmac_f32_e32 v94, v58, v198
	v_add_f32_e32 v25, v25, v94
	v_add_f32_e32 v1, v1, v25
	s_waitcnt lgkmcnt(11)
	v_mul_f32_e32 v25, v75, v201
	ds_read_b128 v[196:199], v105 offset:26624
	v_fmac_f32_e32 v25, v74, v200
	v_mul_f32_e32 v90, v65, v203
	v_fmac_f32_e32 v90, v64, v202
	v_add_f32_e32 v25, v25, v90
	v_add_f32_e32 v1, v1, v25
	s_waitcnt lgkmcnt(11)
	v_mul_f32_e32 v25, v79, v205
	ds_read_b128 v[200:203], v105 offset:27648
	v_mul_f32_e32 v90, v67, v207
	v_fmac_f32_e32 v25, v78, v204
	v_fmac_f32_e32 v90, v66, v206
	v_add_f32_e32 v25, v25, v90
	v_add_f32_e32 v1, v1, v25
	v_mov_b32_e32 v25, 0
	s_nop 0
	s_nop 0
	v_add_f32_dpp v1, v1, v1 row_shr:1 row_mask:0xf bank_mask:0xf bound_ctrl:1
	s_nop 1
	v_add_f32_dpp v1, v1, v1 row_shr:2 row_mask:0xf bank_mask:0xf bound_ctrl:1
	s_nop 1
	v_add_f32_dpp v1, v1, v1 row_shr:4 row_mask:0xf bank_mask:0xf bound_ctrl:1
	s_nop 1
	v_add_f32_dpp v1, v1, v1 row_shr:8 row_mask:0xf bank_mask:0xf bound_ctrl:1
	s_nop 1
	v_mov_b32_dpp v25, v1 row_bcast:15 row_mask:0xa bank_mask:0xf
	v_add_f32_e32 v1, v1, v25
	v_mov_b32_e32 v25, 0
	s_nop 1
	v_mov_b32_dpp v25, v1 row_bcast:31 row_mask:0xc bank_mask:0xf
	v_add_f32_e32 v1, v1, v25
	s_nop 0
	s_waitcnt lgkmcnt(11)
	v_mul_f32_e32 v25, v73, v211
	ds_read_b128 v[204:207], v105 offset:28672
	v_readlane_b32 s38, v1, 63
	v_mul_f32_e32 v1, v85, v209
	v_fmac_f32_e32 v1, v84, v208
	v_fmac_f32_e32 v25, v72, v210
	v_add_f32_e32 v1, v1, v25
	s_waitcnt lgkmcnt(11)
	v_mul_f32_e32 v25, v89, v213
	ds_read_b128 v[208:211], v105 offset:29696
	v_fmac_f32_e32 v25, v88, v212
	v_mul_f32_e32 v94, v63, v215
	v_fmac_f32_e32 v94, v62, v214
	v_add_f32_e32 v1, 0, v1
	v_add_f32_e32 v25, v25, v94
	v_add_f32_e32 v1, v1, v25
	s_waitcnt lgkmcnt(11)
; #define LAS __attribute__((address_space(3)))
; __device__ __forceinline__ float wave_sum(float v) { return lane63(scan64<false>(v)); }
; template <int YMODE, int EXTRA, bool NORM_OUT, bool XN8  , bool XIN_BF = false  , bool XOUT_BF = false  > ...
;     ...
;                     for (int e = 0; e < 8; ++e) { float s = 0.f;
; #pragma unroll
;                         for (int j = 0; j < 8; ++j) { const f32x4 w = *(const LAS f32x4*)(we + e * D + 256 * j + 4 * F.lane); s += (x[j][0] * w[0] + x[j][1] * w[1]) + (x[j][2] * w[2] + x[j][3] * w[3]); }
;                         d8[e] = wave_sum(s); asm volatile("" ::: "memory"); }
	v_mul_f32_e32 v25, v81, v217
	ds_read_b128 v[212:215], v105 offset:30720
	v_fmac_f32_e32 v25, v80, v216
	v_mul_f32_e32 v90, v71, v219
	v_fmac_f32_e32 v90, v70, v218
	v_add_f32_e32 v25, v25, v90
	v_add_f32_e32 v1, v1, v25
	s_waitcnt lgkmcnt(11)
	v_mul_f32_e32 v25, v87, v221
	ds_read_b128 v[216:219], v105 offset:31744
	v_fmac_f32_e32 v25, v86, v220
	v_mul_f32_e32 v94, v61, v223
	v_fmac_f32_e32 v94, v60, v222
	v_add_f32_e32 v25, v25, v94
	v_add_f32_e32 v1, v1, v25
	s_waitcnt lgkmcnt(11)
	v_mul_f32_e32 v25, v77, v225
	ds_read_b128 v[220:223], v105 offset:32768
	v_fmac_f32_e32 v25, v76, v224
	v_mul_f32_e32 v90, v69, v227
	v_fmac_f32_e32 v90, v68, v226
	v_add_f32_e32 v25, v25, v90
	v_add_f32_e32 v1, v1, v25
	s_waitcnt lgkmcnt(11)
	v_mul_f32_e32 v25, v83, v229
	ds_read_b128 v[224:227], v105 offset:33792
	v_fmac_f32_e32 v25, v82, v228
	v_mul_f32_e32 v94, v59, v231
	v_fmac_f32_e32 v94, v58, v230
	v_add_f32_e32 v25, v25, v94
	v_add_f32_e32 v1, v1, v25
	s_waitcnt lgkmcnt(11)
	v_mul_f32_e32 v25, v75, v233
	ds_read_b128 v[228:231], v105 offset:34816
	v_fmac_f32_e32 v25, v74, v232
	v_mul_f32_e32 v90, v65, v235
	v_fmac_f32_e32 v90, v64, v234
	v_add_f32_e32 v25, v25, v90
	v_add_f32_e32 v1, v1, v25
	s_waitcnt lgkmcnt(11)
	v_mul_f32_e32 v25, v79, v241
	ds_read_b128 v[232:235], v105 offset:35840
	v_mul_f32_e32 v90, v67, v243
	v_fmac_f32_e32 v25, v78, v240
	v_fmac_f32_e32 v90, v66, v242
	v_add_f32_e32 v25, v25, v90
	v_add_f32_e32 v1, v1, v25
	v_mov_b32_e32 v25, 0
	s_nop 0
	s_nop 0
	v_add_f32_dpp v1, v1, v1 row_shr:1 row_mask:0xf bank_mask:0xf bound_ctrl:1
	s_nop 1
	v_add_f32_dpp v1, v1, v1 row_shr:2 row_mask:0xf bank_mask:0xf bound_ctrl:1
	s_nop 1
	v_add_f32_dpp v1, v1, v1 row_shr:4 row_mask:0xf bank_mask:0xf bound_ctrl:1
	s_nop 1
	v_add_f32_dpp v1, v1, v1 row_shr:8 row_mask:0xf bank_mask:0xf bound_ctrl:1
	s_nop 1
	v_mov_b32_dpp v25, v1 row_bcast:15 row_mask:0xa bank_mask:0xf
	v_add_f32_e32 v1, v1, v25
	v_mov_b32_e32 v25, 0
	s_nop 1
	v_mov_b32_dpp v25, v1 row_bcast:31 row_mask:0xc bank_mask:0xf
	v_add_f32_e32 v1, v1, v25
	s_nop 0
	s_waitcnt lgkmcnt(11)
	v_mul_f32_e32 v25, v73, v247
	ds_read_b128 v[240:243], v105 offset:36864
	v_readlane_b32 s39, v1, 63
	v_mul_f32_e32 v1, v85, v245
	v_fmac_f32_e32 v1, v84, v244
	v_fmac_f32_e32 v25, v72, v246
	v_add_f32_e32 v1, v1, v25
	s_waitcnt lgkmcnt(11)
	v_mul_f32_e32 v25, v89, v249
	ds_read_b128 v[244:247], v105 offset:37888
	v_fmac_f32_e32 v25, v88, v248
	v_mul_f32_e32 v94, v63, v251
	v_fmac_f32_e32 v94, v62, v250
	v_add_f32_e32 v1, 0, v1
	v_add_f32_e32 v25, v25, v94
	v_add_f32_e32 v1, v1, v25
	s_waitcnt lgkmcnt(11)
	v_mul_f32_e32 v25, v81, v197
	ds_read_b128 v[248:251], v105 offset:38912
	v_fmac_f32_e32 v25, v80, v196
	v_mul_f32_e32 v90, v71, v199
	v_fmac_f32_e32 v90, v70, v198
	v_add_f32_e32 v25, v25, v90
	v_add_f32_e32 v1, v1, v25
	s_waitcnt lgkmcnt(11)
	v_mul_f32_e32 v25, v87, v201
	ds_read_b128 v[196:199], v105 offset:39936
	v_fmac_f32_e32 v25, v86, v200
	v_mul_f32_e32 v94, v61, v203
	v_fmac_f32_e32 v94, v60, v202
	v_add_f32_e32 v25, v25, v94
	v_add_f32_e32 v1, v1, v25
	s_waitcnt lgkmcnt(11)
	v_mul_f32_e32 v25, v77, v205
	ds_read_b128 v[200:203], v105 offset:40960
	v_fmac_f32_e32 v25, v76, v204
	v_mul_f32_e32 v90, v69, v207
	v_fmac_f32_e32 v90, v68, v206
	v_add_f32_e32 v25, v25, v90
	v_add_f32_e32 v1, v1, v25
	s_waitcnt lgkmcnt(11)
	v_mul_f32_e32 v25, v83, v209
	ds_read_b128 v[204:207], v105 offset:41984
	v_fmac_f32_e32 v25, v82, v208
	v_mul_f32_e32 v94, v59, v211
	v_fmac_f32_e32 v94, v58, v210
	v_add_f32_e32 v25, v25, v94
	v_add_f32_e32 v1, v1, v25
	s_waitcnt lgkmcnt(11)
	v_mul_f32_e32 v25, v75, v213
	ds_read_b128 v[208:211], v105 offset:43008
	v_fmac_f32_e32 v25, v74, v212
	v_mul_f32_e32 v90, v65, v215
	v_fmac_f32_e32 v90, v64, v214
	v_add_f32_e32 v25, v25, v90
	v_add_f32_e32 v1, v1, v25
	s_waitcnt lgkmcnt(11)
	v_mul_f32_e32 v25, v79, v217
	ds_read_b128 v[212:215], v105 offset:44032
	v_mul_f32_e32 v90, v67, v219
	v_fmac_f32_e32 v25, v78, v216
	v_fmac_f32_e32 v90, v66, v218
	v_add_f32_e32 v25, v25, v90
	v_add_f32_e32 v1, v1, v25
	v_mov_b32_e32 v25, 0
	s_nop 0
	s_nop 0
	v_add_f32_dpp v1, v1, v1 row_shr:1 row_mask:0xf bank_mask:0xf bound_ctrl:1
	s_nop 1
	v_add_f32_dpp v1, v1, v1 row_shr:2 row_mask:0xf bank_mask:0xf bound_ctrl:1
	s_nop 1
	v_add_f32_dpp v1, v1, v1 row_shr:4 row_mask:0xf bank_mask:0xf bound_ctrl:1
	s_nop 1
	v_add_f32_dpp v1, v1, v1 row_shr:8 row_mask:0xf bank_mask:0xf bound_ctrl:1
	s_nop 1
	v_mov_b32_dpp v25, v1 row_bcast:15 row_mask:0xa bank_mask:0xf
	v_add_f32_e32 v1, v1, v25
	v_mov_b32_e32 v25, 0
	s_nop 1
	v_mov_b32_dpp v25, v1 row_bcast:31 row_mask:0xc bank_mask:0xf
	v_add_f32_e32 v1, v1, v25
	s_nop 0
	s_waitcnt lgkmcnt(11)
	v_mul_f32_e32 v25, v73, v223
	ds_read_b128 v[216:219], v105 offset:45056
	v_readlane_b32 s62, v1, 63
	v_mul_f32_e32 v1, v85, v221
	v_fmac_f32_e32 v1, v84, v220
	v_fmac_f32_e32 v25, v72, v222
	v_add_f32_e32 v1, v1, v25
	s_waitcnt lgkmcnt(11)
	v_mul_f32_e32 v25, v89, v225
	ds_read_b128 v[220:223], v105 offset:46080
	v_fmac_f32_e32 v25, v88, v224
	v_mul_f32_e32 v94, v63, v227
	v_fmac_f32_e32 v94, v62, v226
	v_add_f32_e32 v1, 0, v1
	v_add_f32_e32 v25, v25, v94
	v_add_f32_e32 v1, v1, v25
	s_waitcnt lgkmcnt(11)
	v_mul_f32_e32 v25, v81, v229
	ds_read_b128 v[224:227], v105 offset:47104
	v_fmac_f32_e32 v25, v80, v228
	v_mul_f32_e32 v90, v71, v231
	v_fmac_f32_e32 v90, v70, v230
	v_add_f32_e32 v25, v25, v90
	v_add_f32_e32 v1, v1, v25
	s_waitcnt lgkmcnt(11)
	v_mul_f32_e32 v25, v87, v233
	ds_read_b128 v[228:231], v105 offset:48128
	v_fmac_f32_e32 v25, v86, v232
	v_mul_f32_e32 v94, v61, v235
	v_fmac_f32_e32 v94, v60, v234
	v_add_f32_e32 v25, v25, v94
	v_add_f32_e32 v1, v1, v25
	s_waitcnt lgkmcnt(11)
; #define LAS __attribute__((address_space(3)))
; __device__ __forceinline__ float wave_sum(float v) { return lane63(scan64<false>(v)); }
; template <int YMODE, int EXTRA, bool NORM_OUT, bool XN8  , bool XIN_BF = false  , bool XOUT_BF = false  > ...
;     ...
;                     for (int e = 0; e < 8; ++e) { float s = 0.f;
; #pragma unroll
;                         for (int j = 0; j < 8; ++j) { const f32x4 w = *(const LAS f32x4*)(we + e * D + 256 * j + 4 * F.lane); s += (x[j][0] * w[0] + x[j][1] * w[1]) + (x[j][2] * w[2] + x[j][3] * w[3]); }
;                         d8[e] = wave_sum(s); asm volatile("" ::: "memory"); }
	v_mul_f32_e32 v25, v77, v241
	ds_read_b128 v[232:235], v105 offset:49152
	v_fmac_f32_e32 v25, v76, v240
	v_mul_f32_e32 v90, v69, v243
	v_fmac_f32_e32 v90, v68, v242
	v_add_f32_e32 v25, v25, v90
	v_add_f32_e32 v1, v1, v25
	s_waitcnt lgkmcnt(11)
	v_mul_f32_e32 v25, v83, v245
	ds_read_b128 v[240:243], v105 offset:50176
	v_fmac_f32_e32 v25, v82, v244
	v_mul_f32_e32 v94, v59, v247
	v_fmac_f32_e32 v94, v58, v246
	v_add_f32_e32 v25, v25, v94
	v_add_f32_e32 v1, v1, v25
	s_waitcnt lgkmcnt(11)
	v_mul_f32_e32 v25, v75, v249
	ds_read_b128 v[244:247], v105 offset:51200
	v_fmac_f32_e32 v25, v74, v248
	v_mul_f32_e32 v90, v65, v251
	v_fmac_f32_e32 v90, v64, v250
	v_add_f32_e32 v25, v25, v90
	v_add_f32_e32 v1, v1, v25
	s_waitcnt lgkmcnt(11)
	v_mul_f32_e32 v25, v79, v197
	ds_read_b128 v[248:251], v105 offset:52224
	v_mul_f32_e32 v90, v67, v199
	v_fmac_f32_e32 v25, v78, v196
	v_fmac_f32_e32 v90, v66, v198
	v_add_f32_e32 v25, v25, v90
	v_add_f32_e32 v1, v1, v25
	v_mov_b32_e32 v25, 0
	s_nop 0
	s_nop 0
	v_add_f32_dpp v1, v1, v1 row_shr:1 row_mask:0xf bank_mask:0xf bound_ctrl:1
	s_nop 1
	v_add_f32_dpp v1, v1, v1 row_shr:2 row_mask:0xf bank_mask:0xf bound_ctrl:1
	s_nop 1
	v_add_f32_dpp v1, v1, v1 row_shr:4 row_mask:0xf bank_mask:0xf bound_ctrl:1
	s_nop 1
	v_add_f32_dpp v1, v1, v1 row_shr:8 row_mask:0xf bank_mask:0xf bound_ctrl:1
	s_nop 1
	v_mov_b32_dpp v25, v1 row_bcast:15 row_mask:0xa bank_mask:0xf
	v_add_f32_e32 v1, v1, v25
	v_mov_b32_e32 v25, 0
	s_nop 1
	v_mov_b32_dpp v25, v1 row_bcast:31 row_mask:0xc bank_mask:0xf
	v_add_f32_e32 v1, v1, v25
	s_nop 0
	s_waitcnt lgkmcnt(11)
	v_mul_f32_e32 v25, v73, v203
	ds_read_b128 v[196:199], v105 offset:53248
	v_readlane_b32 s63, v1, 63
	v_mul_f32_e32 v1, v85, v201
	v_fmac_f32_e32 v1, v84, v200
	v_fmac_f32_e32 v25, v72, v202
	v_add_f32_e32 v1, v1, v25
	s_waitcnt lgkmcnt(11)
	v_mul_f32_e32 v25, v89, v205
	ds_read_b128 v[200:203], v105 offset:54272
	v_fmac_f32_e32 v25, v88, v204
	v_mul_f32_e32 v94, v63, v207
	v_fmac_f32_e32 v94, v62, v206
	v_add_f32_e32 v1, 0, v1
	v_add_f32_e32 v25, v25, v94
	v_add_f32_e32 v1, v1, v25
	s_waitcnt lgkmcnt(11)
	v_mul_f32_e32 v25, v81, v209
	ds_read_b128 v[204:207], v105 offset:55296
	v_fmac_f32_e32 v25, v80, v208
	v_mul_f32_e32 v90, v71, v211
	v_fmac_f32_e32 v90, v70, v210
	v_add_f32_e32 v25, v25, v90
	v_add_f32_e32 v1, v1, v25
	s_waitcnt lgkmcnt(11)
	v_mul_f32_e32 v25, v87, v213
	ds_read_b128 v[208:211], v105 offset:56320
	v_fmac_f32_e32 v25, v86, v212
	v_mul_f32_e32 v94, v61, v215
	v_fmac_f32_e32 v94, v60, v214
	v_add_f32_e32 v25, v25, v94
	v_add_f32_e32 v1, v1, v25
	s_waitcnt lgkmcnt(11)
	v_mul_f32_e32 v25, v77, v217
	ds_read_b128 v[212:215], v105 offset:57344
	v_fmac_f32_e32 v25, v76, v216
	v_mul_f32_e32 v90, v69, v219
	v_fmac_f32_e32 v90, v68, v218
	v_add_f32_e32 v25, v25, v90
	v_add_f32_e32 v1, v1, v25
	s_waitcnt lgkmcnt(11)
	v_mul_f32_e32 v25, v83, v221
	ds_read_b128 v[216:219], v105 offset:58368
	v_fmac_f32_e32 v25, v82, v220
	v_mul_f32_e32 v94, v59, v223
	v_fmac_f32_e32 v94, v58, v222
	v_add_f32_e32 v25, v25, v94
	v_add_f32_e32 v1, v1, v25
	s_waitcnt lgkmcnt(11)
	v_mul_f32_e32 v25, v75, v225
	ds_read_b128 v[220:223], v105 offset:59392
	v_fmac_f32_e32 v25, v74, v224
	v_mul_f32_e32 v90, v65, v227
	v_fmac_f32_e32 v90, v64, v226
	v_add_f32_e32 v25, v25, v90
	v_add_f32_e32 v1, v1, v25
	s_waitcnt lgkmcnt(11)
	v_mul_f32_e32 v25, v79, v229
	ds_read_b128 v[224:227], v105 offset:60416
	v_mul_f32_e32 v90, v67, v231
	v_fmac_f32_e32 v25, v78, v228
	v_fmac_f32_e32 v90, v66, v230
	v_add_f32_e32 v25, v25, v90
	v_add_f32_e32 v1, v1, v25
	v_mov_b32_e32 v25, 0
	s_nop 0
	s_nop 0
	v_add_f32_dpp v1, v1, v1 row_shr:1 row_mask:0xf bank_mask:0xf bound_ctrl:1
	s_nop 1
	v_add_f32_dpp v1, v1, v1 row_shr:2 row_mask:0xf bank_mask:0xf bound_ctrl:1
	s_nop 1
	v_add_f32_dpp v1, v1, v1 row_shr:4 row_mask:0xf bank_mask:0xf bound_ctrl:1
	s_nop 1
	v_add_f32_dpp v1, v1, v1 row_shr:8 row_mask:0xf bank_mask:0xf bound_ctrl:1
	s_nop 1
	v_mov_b32_dpp v25, v1 row_bcast:15 row_mask:0xa bank_mask:0xf
	v_add_f32_e32 v1, v1, v25
	v_mov_b32_e32 v25, 0
	s_nop 1
	v_mov_b32_dpp v25, v1 row_bcast:31 row_mask:0xc bank_mask:0xf
	v_add_f32_e32 v1, v1, v25
	s_nop 0
	s_waitcnt lgkmcnt(11)
	v_mul_f32_e32 v25, v73, v235
	ds_read_b128 v[228:231], v105 offset:61440
	v_readlane_b32 s66, v1, 63
	v_mul_f32_e32 v1, v85, v233
	v_fmac_f32_e32 v1, v84, v232
	v_fmac_f32_e32 v25, v72, v234
	v_add_f32_e32 v1, v1, v25
	s_waitcnt lgkmcnt(11)
	v_mul_f32_e32 v25, v89, v241
	ds_read_b128 v[232:235], v105 offset:62464
	v_fmac_f32_e32 v25, v88, v240
	v_mul_f32_e32 v94, v63, v243
	v_fmac_f32_e32 v94, v62, v242
	v_add_f32_e32 v1, 0, v1
	v_add_f32_e32 v25, v25, v94
	v_add_f32_e32 v1, v1, v25
	s_waitcnt lgkmcnt(11)
	v_mul_f32_e32 v25, v81, v245
	ds_read_b128 v[240:243], v105 offset:63488
	v_fmac_f32_e32 v25, v80, v244
	v_mul_f32_e32 v90, v71, v247
	v_fmac_f32_e32 v90, v70, v246
	v_add_f32_e32 v25, v25, v90
	v_add_f32_e32 v1, v1, v25
	s_waitcnt lgkmcnt(11)
	v_mul_f32_e32 v25, v87, v249
	ds_read_b128 v[244:247], v105 offset:64512
	v_fmac_f32_e32 v25, v86, v248
	v_mul_f32_e32 v94, v61, v251
	v_fmac_f32_e32 v94, v60, v250
	v_add_f32_e32 v25, v25, v94
	v_add_f32_e32 v1, v1, v25
	s_waitcnt lgkmcnt(11)
; #define LAS __attribute__((address_space(3)))
; __device__ __forceinline__ float wave_sum(float v) { return lane63(scan64<false>(v)); }
; template <int YMODE, int EXTRA, bool NORM_OUT, bool XN8  , bool XIN_BF = false  , bool XOUT_BF = false  > ...
;     ...
;                     for (int e = 0; e < 8; ++e) { float s = 0.f;
; #pragma unroll
;                         for (int j = 0; j < 8; ++j) { const f32x4 w = *(const LAS f32x4*)(we + e * D + 256 * j + 4 * F.lane); s += (x[j][0] * w[0] + x[j][1] * w[1]) + (x[j][2] * w[2] + x[j][3] * w[3]); }
;                         d8[e] = wave_sum(s); asm volatile("" ::: "memory"); }
;                     if (EXTRA == 1) {
;                         float v = 0.f;
; #pragma unroll
;                         for (int e = 0; e < 8; ++e) v = (F.lane == e) ? d8[e] : v;
;                         if (F.lane < 8) { const float bb = (F.lane < 4) ? bi[F.lane] : bfg[F.lane - 4]; const float z = 15.f * tanhf((v + bb) * (1.f / 15.f));
;                             const float o = (F.lane < 4) ? z : (fminf(z, 0.f) - log1pf(expf(-fabsf(z)))); gates_out[row * 8 + F.lane] = o; }
	v_mul_f32_e32 v25, v77, v197
	v_fmac_f32_e32 v25, v76, v196
	v_mul_f32_e32 v90, v69, v199
	v_fmac_f32_e32 v90, v68, v198
	v_add_f32_e32 v25, v25, v90
	v_add_f32_e32 v1, v1, v25
	s_waitcnt lgkmcnt(10)
	v_mul_f32_e32 v25, v83, v201
	v_fmac_f32_e32 v25, v82, v200
	v_mul_f32_e32 v94, v59, v203
	v_fmac_f32_e32 v94, v58, v202
	v_add_f32_e32 v25, v25, v94
	v_add_f32_e32 v1, v1, v25
	s_waitcnt lgkmcnt(9)
	v_mul_f32_e32 v25, v75, v205
	v_fmac_f32_e32 v25, v74, v204
	v_mul_f32_e32 v90, v65, v207
	v_fmac_f32_e32 v90, v64, v206
	v_add_f32_e32 v25, v25, v90
	v_add_f32_e32 v1, v1, v25
	s_waitcnt lgkmcnt(8)
	v_mul_f32_e32 v25, v79, v209
	v_mul_f32_e32 v90, v67, v211
	v_fmac_f32_e32 v25, v78, v208
	v_fmac_f32_e32 v90, v66, v210
	v_add_f32_e32 v25, v25, v90
	v_add_f32_e32 v1, v1, v25
	v_mov_b32_e32 v25, 0
	s_nop 0
	s_nop 0
	v_add_f32_dpp v1, v1, v1 row_shr:1 row_mask:0xf bank_mask:0xf bound_ctrl:1
	s_nop 0
	s_waitcnt lgkmcnt(6)
	v_mul_f32_e32 v63, v63, v219
	v_add_f32_dpp v1, v1, v1 row_shr:2 row_mask:0xf bank_mask:0xf bound_ctrl:1
	v_fmac_f32_e32 v63, v62, v218
	s_nop 0
	v_add_f32_dpp v1, v1, v1 row_shr:4 row_mask:0xf bank_mask:0xf bound_ctrl:1
	s_nop 1
	v_add_f32_dpp v1, v1, v1 row_shr:8 row_mask:0xf bank_mask:0xf bound_ctrl:1
	s_nop 1
	v_mov_b32_dpp v25, v1 row_bcast:15 row_mask:0xa bank_mask:0xf
	v_add_f32_e32 v1, v1, v25
	v_mov_b32_e32 v25, 0
	s_nop 1
	v_mov_b32_dpp v25, v1 row_bcast:31 row_mask:0xc bank_mask:0xf
	v_add_f32_e32 v1, v1, v25
	v_mul_f32_e32 v25, v73, v215
	v_readlane_b32 s67, v1, 63
	v_mul_f32_e32 v1, v85, v213
	v_fmac_f32_e32 v1, v84, v212
	v_fmac_f32_e32 v25, v72, v214
	v_add_f32_e32 v1, v1, v25
	v_mul_f32_e32 v25, v89, v217
	v_fmac_f32_e32 v25, v88, v216
	v_add_f32_e32 v1, 0, v1
	v_add_f32_e32 v25, v25, v63
	v_add_f32_e32 v1, v1, v25
	s_waitcnt lgkmcnt(5)
	v_mul_f32_e32 v25, v81, v221
	v_mul_f32_e32 v62, v71, v223
	v_fmac_f32_e32 v25, v80, v220
	v_fmac_f32_e32 v62, v70, v222
	v_add_f32_e32 v25, v25, v62
	v_add_f32_e32 v1, v1, v25
	s_waitcnt lgkmcnt(4)
	v_mul_f32_e32 v25, v87, v225
	v_mul_f32_e32 v61, v61, v227
	v_fmac_f32_e32 v25, v86, v224
	v_fmac_f32_e32 v61, v60, v226
	v_add_f32_e32 v25, v25, v61
	v_add_f32_e32 v1, v1, v25
	s_waitcnt lgkmcnt(3)
	v_mul_f32_e32 v25, v77, v229
	v_mul_f32_e32 v69, v69, v231
	v_fmac_f32_e32 v25, v76, v228
	v_fmac_f32_e32 v69, v68, v230
	v_add_f32_e32 v25, v25, v69
	v_add_f32_e32 v1, v1, v25
	s_waitcnt lgkmcnt(2)
	v_mul_f32_e32 v25, v83, v233
	v_mul_f32_e32 v59, v59, v235
	v_fmac_f32_e32 v25, v82, v232
	v_fmac_f32_e32 v59, v58, v234
	v_add_f32_e32 v25, v25, v59
	v_add_f32_e32 v1, v1, v25
	s_waitcnt lgkmcnt(1)
	v_mul_f32_e32 v25, v75, v241
	v_mul_f32_e32 v62, v65, v243
	v_fmac_f32_e32 v25, v74, v240
	v_fmac_f32_e32 v62, v64, v242
	v_add_f32_e32 v25, v25, v62
	v_add_f32_e32 v1, v1, v25
	s_waitcnt lgkmcnt(0)
	v_mul_f32_e32 v25, v79, v245
	v_fmac_f32_e32 v25, v78, v244
	v_mul_f32_e32 v58, v67, v247
	v_fmac_f32_e32 v58, v66, v246
	v_add_f32_e32 v25, v25, v58
	v_add_f32_e32 v1, v1, v25
	v_mov_b32_e32 v25, 0
	s_nop 0
	v_add_f32_dpp v1, v1, v1 row_shr:1 row_mask:0xf bank_mask:0xf bound_ctrl:1
	s_nop 1
	v_add_f32_dpp v1, v1, v1 row_shr:2 row_mask:0xf bank_mask:0xf bound_ctrl:1
	s_nop 1
	v_add_f32_dpp v1, v1, v1 row_shr:4 row_mask:0xf bank_mask:0xf bound_ctrl:1
	s_nop 1
	v_add_f32_dpp v1, v1, v1 row_shr:8 row_mask:0xf bank_mask:0xf bound_ctrl:1
	s_nop 1
	v_mov_b32_dpp v25, v1 row_bcast:15 row_mask:0xa bank_mask:0xf
	v_add_f32_e32 v1, v1, v25
	v_mov_b32_e32 v25, 0
	s_nop 1
	v_mov_b32_dpp v25, v1 row_bcast:31 row_mask:0xc bank_mask:0xf
	v_add_f32_e32 v1, v1, v25
	s_nop 0
	v_readlane_b32 s68, v1, 63
	s_and_saveexec_b64 s[26:27], s[8:9]
	s_cbranch_execz .LBB0_1306
	v_mov_b32_e32 v1, s34
	v_cndmask_b32_e64 v1, 0, v1, s[6:7]
	v_mov_b32_e32 v25, s38
	v_cndmask_b32_e64 v1, v1, v25, s[22:23]
	v_mov_b32_e32 v25, s39
	v_cndmask_b32_e64 v1, v1, v25, s[20:21]
	v_mov_b32_e32 v25, s62
	v_cndmask_b32_e64 v1, v1, v25, s[18:19]
	v_mov_b32_e32 v25, s63
	v_cndmask_b32_e64 v1, v1, v25, s[16:17]
	v_mov_b32_e32 v25, s66
	v_cndmask_b32_e64 v1, v1, v25, s[14:15]
	v_mov_b32_e32 v25, s67
	v_cndmask_b32_e64 v1, v1, v25, s[12:13]
	v_mov_b32_e32 v25, s68
	v_cndmask_b32_e64 v1, v1, v25, s[10:11]
	global_load_dword v25, v[18:19], off
	s_mov_b32 s34, 0x3f200000
	s_waitcnt vmcnt(0) lgkmcnt(0)
	v_add_f32_e32 v1, v1, v25
	v_mul_f32_e32 v1, 0x3d888889, v1
	v_cmp_nlt_f32_e64 s[38:39], |v1|, s34
	s_and_saveexec_b64 s[62:63], s[38:39]
	s_xor_b64 s[38:39], exec, s[62:63]
	s_cbranch_execz .LBB0_1314
	v_add_f32_e64 v25, |v1|, |v1|
	v_mul_f32_e32 v58, 0x3fb8aa3b, v25
	v_rndne_f32_e32 v59, v58
	s_mov_b32 s34, 0x3fb8aa3b
	v_sub_f32_e32 v60, v58, v59
	v_fma_f32 v58, v25, s34, -v58
	v_fmac_f32_e32 v58, 0x32a5705f, v25
	v_add_f32_e32 v58, v60, v58
	v_cvt_i32_f32_e32 v59, v59
	v_exp_f32_e32 v58, v58
	s_mov_b32 s34, 0xc2ce8ed0
	v_cmp_ngt_f32_e32 vcc, s34, v25
	v_ldexp_f32 v58, v58, v59
	s_nop 0
	v_cndmask_b32_e32 v58, 0, v58, vcc
	v_cmp_nlt_f32_e32 vcc, s44, v25
	s_nop 1
	v_cndmask_b32_e32 v25, v111, v58, vcc
	v_add_f32_e32 v25, 1.0, v25
	v_rcp_f32_e32 v25, v25
	s_nop 0
	v_fma_f32 v25, v25, -2.0, 1.0

; #define LAS __attribute__((address_space(3)))
; template <int YMODE, int EXTRA, bool NORM_OUT, bool XN8  , bool XIN_BF = false  , bool XOUT_BF = false  > ...
;     ...
;                     const float inv = am > 0.f ? 127.f / am : 0.f;
;                     if (F.lane == 0) { rowmax[row] = am; if (EXTRA == 2) route[384 + rl] = am; }
; #pragma unroll
;                     for (int j = 0; j < 8; ++j) *(unsigned*)((unsigned char*)XN + row * D + 256 * j + 4 * F.lane) = pack_i8x4(x[j][0] * inv, x[j][1] * inv, x[j][2] * inv, x[j][3] * inv);
;     ...
;                     for (int e = 0; e < 8; ++e) { float s = 0.f;
; #pragma unroll
;                         for (int j = 0; j < 8; ++j) { const f32x4 w = *(const LAS f32x4*)(we + e * D + 256 * j + 4 * F.lane); s += (x[j][0] * w[0] + x[j][1] * w[1]) + (x[j][2] * w[2] + x[j][3] * w[3]); }
.LBB0_2181:
	s_or_b64 exec, exec, s[12:13]
	ds_read_b128 v[196:199], v118
	ds_read_b128 v[200:203], v118 offset:1024
	ds_read_b128 v[204:207], v118 offset:2048
	ds_read_b128 v[208:211], v118 offset:3072
	ds_read_b128 v[212:215], v118 offset:4096
	ds_read_b128 v[216:219], v118 offset:5120
	ds_read_b128 v[220:223], v118 offset:6144
	ds_read_b128 v[224:227], v118 offset:7168
	ds_read_b128 v[228:231], v118 offset:8192
	ds_read_b128 v[232:235], v118 offset:9216
	ds_read_b128 v[240:243], v118 offset:10240
	ds_read_b128 v[244:247], v118 offset:11264
	v_div_scale_f32 v2, s[16:17], s14, s14, v125
	v_rcp_f32_e32 v88, v2
	s_mov_b32 s15, 0x42fe0000
	v_cmp_gt_f32_e64 s[12:13], s14, 0
	s_lshl_b64 s[0:1], s[0:1], 11
	v_fma_f32 v89, -v2, v88, 1.0
	v_fmac_f32_e32 v88, v89, v88
	v_mov_b32_e32 v89, s14
	v_div_scale_f32 v89, vcc, s15, v89, s15
	v_mul_f32_e32 v90, v89, v88
	v_fma_f32 v91, -v2, v90, v89
	v_fmac_f32_e32 v90, v91, v88
	v_fma_f32 v2, -v2, v90, v89
	v_div_fmas_f32 v2, v2, v88, v90
	v_div_fixup_f32 v2, v2, s14, v125
	v_cndmask_b32_e64 v2, 0, v2, s[12:13]
	v_mul_f32_e32 v89, v87, v2
	v_mul_f32_e32 v88, v86, v2
	v_mul_f32_e32 v90, v84, v2
	v_mul_f32_e32 v91, v85, v2
	v_med3_f32 v89, v89, s46, v125
	v_med3_f32 v88, v88, s46, v125
	v_rndne_f32_e32 v89, v89
	v_med3_f32 v90, v90, s46, v125
	v_med3_f32 v91, v91, s46, v125
	v_rndne_f32_e32 v88, v88
	v_cvt_i32_f32_e32 v89, v89
	v_rndne_f32_e32 v90, v90
	v_rndne_f32_e32 v91, v91
	v_cvt_i32_f32_e32 v88, v88
	v_cvt_i32_f32_sdwa v90, v90 dst_sel:WORD_1 dst_unused:UNUSED_PAD src0_sel:DWORD
	v_cvt_i32_f32_e32 v91, v91
	v_lshlrev_b32_e32 v89, 8, v89
	v_and_b32_e32 v89, 0xff00, v89
	v_and_b32_e32 v90, 0xff0000, v90
	v_perm_b32 v88, v91, v88, s47
	v_or3_b32 v90, v88, v89, v90
	v_lshl_add_u64 v[88:89], v[22:23], 0, s[0:1]
	v_mul_f32_e32 v91, v83, v2
	global_store_dword v[88:89], v90, off
	v_mul_f32_e32 v90, v82, v2
	v_mul_f32_e32 v92, v80, v2
	v_mul_f32_e32 v93, v81, v2
	v_med3_f32 v91, v91, s46, v125
	v_med3_f32 v90, v90, s46, v125
	v_rndne_f32_e32 v91, v91
	v_med3_f32 v92, v92, s46, v125
	v_med3_f32 v93, v93, s46, v125
	v_rndne_f32_e32 v90, v90
	v_cvt_i32_f32_e32 v91, v91
	v_rndne_f32_e32 v92, v92
	v_rndne_f32_e32 v93, v93
	v_cvt_i32_f32_e32 v90, v90
	v_cvt_i32_f32_sdwa v92, v92 dst_sel:WORD_1 dst_unused:UNUSED_PAD src0_sel:DWORD
	v_cvt_i32_f32_e32 v93, v93
	v_lshlrev_b32_e32 v91, 8, v91
	v_and_b32_e32 v91, 0xff00, v91
	v_and_b32_e32 v92, 0xff0000, v92
	v_perm_b32 v90, v93, v90, s47
	v_or3_b32 v90, v90, v91, v92
	v_mul_f32_e32 v91, v79, v2
	global_store_dword v[88:89], v90, off offset:256
	v_mul_f32_e32 v90, v78, v2
	v_mul_f32_e32 v92, v76, v2
	v_mul_f32_e32 v93, v77, v2
	v_med3_f32 v91, v91, s46, v125
	v_med3_f32 v90, v90, s46, v125
	v_rndne_f32_e32 v91, v91
	v_med3_f32 v92, v92, s46, v125
	v_med3_f32 v93, v93, s46, v125
	v_rndne_f32_e32 v90, v90
	v_cvt_i32_f32_e32 v91, v91
	v_rndne_f32_e32 v92, v92
	v_rndne_f32_e32 v93, v93
	v_cvt_i32_f32_e32 v90, v90
	v_cvt_i32_f32_sdwa v92, v92 dst_sel:WORD_1 dst_unused:UNUSED_PAD src0_sel:DWORD
	v_cvt_i32_f32_e32 v93, v93
	v_lshlrev_b32_e32 v91, 8, v91
	v_and_b32_e32 v91, 0xff00, v91
	v_and_b32_e32 v92, 0xff0000, v92
	v_perm_b32 v90, v93, v90, s47
	v_or3_b32 v90, v90, v91, v92
	v_mul_f32_e32 v91, v75, v2
	global_store_dword v[88:89], v90, off offset:512
	v_mul_f32_e32 v90, v74, v2
	v_mul_f32_e32 v92, v72, v2
	v_mul_f32_e32 v93, v73, v2
	v_med3_f32 v91, v91, s46, v125
	v_med3_f32 v90, v90, s46, v125
	v_rndne_f32_e32 v91, v91
	v_med3_f32 v92, v92, s46, v125
	v_med3_f32 v93, v93, s46, v125
	v_rndne_f32_e32 v90, v90
	v_cvt_i32_f32_e32 v91, v91
	v_rndne_f32_e32 v92, v92
	v_rndne_f32_e32 v93, v93
	v_cvt_i32_f32_e32 v90, v90
	v_cvt_i32_f32_sdwa v92, v92 dst_sel:WORD_1 dst_unused:UNUSED_PAD src0_sel:DWORD
	v_cvt_i32_f32_e32 v93, v93
	v_lshlrev_b32_e32 v91, 8, v91
	v_and_b32_e32 v91, 0xff00, v91
	v_and_b32_e32 v92, 0xff0000, v92
	v_perm_b32 v90, v93, v90, s47
	v_or3_b32 v90, v90, v91, v92
	v_mul_f32_e32 v91, v71, v2
	global_store_dword v[88:89], v90, off offset:768
	v_mul_f32_e32 v90, v70, v2
	v_mul_f32_e32 v92, v68, v2
	v_mul_f32_e32 v93, v69, v2
	v_med3_f32 v91, v91, s46, v125
	v_med3_f32 v90, v90, s46, v125
	v_rndne_f32_e32 v91, v91
	v_med3_f32 v92, v92, s46, v125
	v_med3_f32 v93, v93, s46, v125
	v_rndne_f32_e32 v90, v90
	v_cvt_i32_f32_e32 v91, v91
	v_rndne_f32_e32 v92, v92
	v_rndne_f32_e32 v93, v93
	v_cvt_i32_f32_e32 v90, v90
	v_cvt_i32_f32_sdwa v92, v92 dst_sel:WORD_1 dst_unused:UNUSED_PAD src0_sel:DWORD
	v_cvt_i32_f32_e32 v93, v93
	v_lshlrev_b32_e32 v91, 8, v91
	v_and_b32_e32 v91, 0xff00, v91
	v_and_b32_e32 v92, 0xff0000, v92
	v_perm_b32 v90, v93, v90, s47
	v_or3_b32 v90, v90, v91, v92
	v_mul_f32_e32 v91, v67, v2
	global_store_dword v[88:89], v90, off offset:1024
	v_mul_f32_e32 v90, v66, v2
	v_mul_f32_e32 v92, v64, v2
	v_mul_f32_e32 v93, v65, v2
	v_med3_f32 v91, v91, s46, v125
	v_med3_f32 v90, v90, s46, v125
	v_rndne_f32_e32 v91, v91
	v_med3_f32 v92, v92, s46, v125
	v_med3_f32 v93, v93, s46, v125
	v_rndne_f32_e32 v90, v90
	v_cvt_i32_f32_e32 v91, v91
	v_rndne_f32_e32 v92, v92
	v_rndne_f32_e32 v93, v93
	v_cvt_i32_f32_e32 v90, v90
	v_cvt_i32_f32_sdwa v92, v92 dst_sel:WORD_1 dst_unused:UNUSED_PAD src0_sel:DWORD
	v_cvt_i32_f32_e32 v93, v93
	v_lshlrev_b32_e32 v91, 8, v91
	v_and_b32_e32 v91, 0xff00, v91
	v_and_b32_e32 v92, 0xff0000, v92
	v_perm_b32 v90, v93, v90, s47
	v_or3_b32 v90, v90, v91, v92
	v_mul_f32_e32 v91, v63, v2
	global_store_dword v[88:89], v90, off offset:1280
	v_mul_f32_e32 v90, v62, v2
	v_mul_f32_e32 v92, v60, v2
	v_mul_f32_e32 v93, v61, v2
	v_med3_f32 v91, v91, s46, v125
	v_med3_f32 v90, v90, s46, v125
	v_rndne_f32_e32 v91, v91
	v_med3_f32 v92, v92, s46, v125
	v_med3_f32 v93, v93, s46, v125
	v_rndne_f32_e32 v90, v90
	v_cvt_i32_f32_e32 v91, v91
	v_rndne_f32_e32 v92, v92
	v_rndne_f32_e32 v93, v93
	v_cvt_i32_f32_e32 v90, v90
	v_cvt_i32_f32_sdwa v92, v92 dst_sel:WORD_1 dst_unused:UNUSED_PAD src0_sel:DWORD
	v_cvt_i32_f32_e32 v93, v93
	v_lshlrev_b32_e32 v91, 8, v91
	v_and_b32_e32 v91, 0xff00, v91
	v_and_b32_e32 v92, 0xff0000, v92
	v_perm_b32 v90, v93, v90, s47
	v_or3_b32 v90, v90, v91, v92
	v_mul_f32_e32 v91, v59, v2
	global_store_dword v[88:89], v90, off offset:1536
	v_mul_f32_e32 v90, v58, v2
	v_mul_f32_e32 v92, v56, v2
	v_mul_f32_e32 v2, v57, v2
	v_med3_f32 v91, v91, s46, v125
	v_med3_f32 v90, v90, s46, v125
	v_rndne_f32_e32 v91, v91
	v_med3_f32 v92, v92, s46, v125
	v_med3_f32 v2, v2, s46, v125
	v_rndne_f32_e32 v90, v90
	v_cvt_i32_f32_e32 v91, v91
	v_rndne_f32_e32 v92, v92
	v_rndne_f32_e32 v2, v2
	v_cvt_i32_f32_e32 v90, v90
	v_cvt_i32_f32_sdwa v92, v92 dst_sel:WORD_1 dst_unused:UNUSED_PAD src0_sel:DWORD
	v_cvt_i32_f32_e32 v2, v2
	v_lshlrev_b32_e32 v91, 8, v91
	v_and_b32_e32 v91, 0xff00, v91
	v_and_b32_e32 v92, 0xff0000, v92
	v_perm_b32 v2, v2, v90, s47
	v_or3_b32 v2, v2, v91, v92
	global_store_dword v[88:89], v2, off offset:1792
	s_nop 0
	s_waitcnt lgkmcnt(12)
; #define LAS __attribute__((address_space(3)))
; __device__ __forceinline__ float wave_sum(float v) { return lane63(scan64<false>(v)); }
; template <int YMODE, int EXTRA, bool NORM_OUT, bool XN8  , bool XIN_BF = false  , bool XOUT_BF = false  > ...
;     ...
;                     for (int e = 0; e < 8; ++e) { float s = 0.f;
; #pragma unroll
;                         for (int j = 0; j < 8; ++j) { const f32x4 w = *(const LAS f32x4*)(we + e * D + 256 * j + 4 * F.lane); s += (x[j][0] * w[0] + x[j][1] * w[1]) + (x[j][2] * w[2] + x[j][3] * w[3]); }
;                         d8[e] = wave_sum(s); asm volatile("" ::: "memory"); }
	s_waitcnt lgkmcnt(11)
	v_mul_f32_e32 v2, v87, v197
	ds_read_b128 v[248:251], v118 offset:12288
	v_fmac_f32_e32 v2, v86, v196
	v_mul_f32_e32 v88, v85, v199
	v_fmac_f32_e32 v88, v84, v198
	v_add_f32_e32 v2, v2, v88
	v_add_f32_e32 v2, 0, v2
	s_waitcnt lgkmcnt(11)
	v_mul_f32_e32 v89, v83, v201
	ds_read_b128 v[196:199], v118 offset:13312
	v_fmac_f32_e32 v89, v82, v200
	v_mul_f32_e32 v88, v81, v203
	v_fmac_f32_e32 v88, v80, v202
	v_add_f32_e32 v88, v89, v88
	v_add_f32_e32 v2, v2, v88
	s_waitcnt lgkmcnt(11)
	v_mul_f32_e32 v89, v79, v205
	ds_read_b128 v[200:203], v118 offset:14336
	v_fmac_f32_e32 v89, v78, v204
	v_mul_f32_e32 v88, v77, v207
	v_fmac_f32_e32 v88, v76, v206
	v_add_f32_e32 v88, v89, v88
	v_add_f32_e32 v2, v2, v88
	s_waitcnt lgkmcnt(11)
	v_mul_f32_e32 v89, v75, v209
	ds_read_b128 v[204:207], v118 offset:15360
	v_fmac_f32_e32 v89, v74, v208
	v_mul_f32_e32 v88, v73, v211
	v_fmac_f32_e32 v88, v72, v210
	v_add_f32_e32 v88, v89, v88
	v_add_f32_e32 v2, v2, v88
	s_waitcnt lgkmcnt(11)
	v_mul_f32_e32 v89, v71, v213
	ds_read_b128 v[208:211], v118 offset:16384
	v_fmac_f32_e32 v89, v70, v212
	v_mul_f32_e32 v88, v69, v215
	v_fmac_f32_e32 v88, v68, v214
	v_add_f32_e32 v88, v89, v88
	v_add_f32_e32 v2, v2, v88
	s_waitcnt lgkmcnt(11)
	v_mul_f32_e32 v89, v67, v217
	ds_read_b128 v[212:215], v118 offset:17408
	v_fmac_f32_e32 v89, v66, v216
	v_mul_f32_e32 v88, v65, v219
	v_fmac_f32_e32 v88, v64, v218
	v_add_f32_e32 v88, v89, v88
	v_add_f32_e32 v2, v2, v88
	s_waitcnt lgkmcnt(11)
	v_mul_f32_e32 v89, v63, v221
	ds_read_b128 v[216:219], v118 offset:18432
	v_fmac_f32_e32 v89, v62, v220
	v_mul_f32_e32 v88, v61, v223
	v_fmac_f32_e32 v88, v60, v222
	v_add_f32_e32 v88, v89, v88
	v_add_f32_e32 v2, v2, v88
	s_waitcnt lgkmcnt(11)
	v_mul_f32_e32 v89, v59, v225
	ds_read_b128 v[220:223], v118 offset:19456
	v_fmac_f32_e32 v89, v58, v224
	v_mul_f32_e32 v88, v57, v227
	v_fmac_f32_e32 v88, v56, v226
	v_add_f32_e32 v88, v89, v88
	v_add_f32_e32 v2, v2, v88
	v_mov_b32_e32 v88, 0
	s_nop 0
	v_add_f32_dpp v2, v2, v2 row_shr:1 row_mask:0xf bank_mask:0xf bound_ctrl:1
	s_nop 1
	v_add_f32_dpp v2, v2, v2 row_shr:2 row_mask:0xf bank_mask:0xf bound_ctrl:1
	s_nop 1
	v_add_f32_dpp v2, v2, v2 row_shr:4 row_mask:0xf bank_mask:0xf bound_ctrl:1
	s_nop 1
	v_add_f32_dpp v2, v2, v2 row_shr:8 row_mask:0xf bank_mask:0xf bound_ctrl:1
	s_nop 1
	v_mov_b32_dpp v88, v2 row_bcast:15 row_mask:0xa bank_mask:0xf
	v_add_f32_e32 v2, v2, v88
	v_mov_b32_e32 v88, 0
	s_nop 1
	v_mov_b32_dpp v88, v2 row_bcast:31 row_mask:0xc bank_mask:0xf
	v_add_f32_e32 v2, v2, v88
	s_nop 0
	v_readlane_b32 s24, v2, 63
	s_nop 0
	s_waitcnt lgkmcnt(11)
	v_mul_f32_e32 v2, v87, v229
	ds_read_b128 v[224:227], v118 offset:20480
	v_fmac_f32_e32 v2, v86, v228
	v_mul_f32_e32 v88, v85, v231
	v_fmac_f32_e32 v88, v84, v230
	v_add_f32_e32 v2, v2, v88
	v_add_f32_e32 v2, 0, v2
	s_waitcnt lgkmcnt(11)
	v_mul_f32_e32 v89, v83, v233
	ds_read_b128 v[228:231], v118 offset:21504
	v_fmac_f32_e32 v89, v82, v232
	v_mul_f32_e32 v88, v81, v235
	v_fmac_f32_e32 v88, v80, v234
	v_add_f32_e32 v88, v89, v88
	v_add_f32_e32 v2, v2, v88
	s_waitcnt lgkmcnt(11)
	v_mul_f32_e32 v89, v79, v241
	ds_read_b128 v[232:235], v118 offset:22528
	v_fmac_f32_e32 v89, v78, v240
	v_mul_f32_e32 v88, v77, v243
	v_fmac_f32_e32 v88, v76, v242
	v_add_f32_e32 v88, v89, v88
	v_add_f32_e32 v2, v2, v88
	s_waitcnt lgkmcnt(11)
	v_mul_f32_e32 v89, v75, v245
	ds_read_b128 v[240:243], v118 offset:23552
	v_fmac_f32_e32 v89, v74, v244
	v_mul_f32_e32 v88, v73, v247
	v_fmac_f32_e32 v88, v72, v246
	v_add_f32_e32 v88, v89, v88
	v_add_f32_e32 v2, v2, v88
	s_waitcnt lgkmcnt(11)
	v_mul_f32_e32 v89, v71, v249
	ds_read_b128 v[244:247], v118 offset:24576
	v_fmac_f32_e32 v89, v70, v248
	v_mul_f32_e32 v88, v69, v251
	v_fmac_f32_e32 v88, v68, v250
	v_add_f32_e32 v88, v89, v88
	v_add_f32_e32 v2, v2, v88
	s_waitcnt lgkmcnt(11)
	v_mul_f32_e32 v89, v67, v197
	ds_read_b128 v[248:251], v118 offset:25600
	v_fmac_f32_e32 v89, v66, v196
	v_mul_f32_e32 v88, v65, v199
	v_fmac_f32_e32 v88, v64, v198
	v_add_f32_e32 v88, v89, v88
	v_add_f32_e32 v2, v2, v88
	s_waitcnt lgkmcnt(11)
	v_mul_f32_e32 v89, v63, v201
	ds_read_b128 v[196:199], v118 offset:26624
	v_fmac_f32_e32 v89, v62, v200
	v_mul_f32_e32 v88, v61, v203
	v_fmac_f32_e32 v88, v60, v202
	v_add_f32_e32 v88, v89, v88
	v_add_f32_e32 v2, v2, v88
	s_waitcnt lgkmcnt(11)
	v_mul_f32_e32 v89, v59, v205
	ds_read_b128 v[200:203], v118 offset:27648
	v_fmac_f32_e32 v89, v58, v204
	v_mul_f32_e32 v88, v57, v207
	v_fmac_f32_e32 v88, v56, v206
	v_add_f32_e32 v88, v89, v88
	v_add_f32_e32 v2, v2, v88
	v_mov_b32_e32 v88, 0
	s_nop 0
	v_add_f32_dpp v2, v2, v2 row_shr:1 row_mask:0xf bank_mask:0xf bound_ctrl:1
	s_nop 1
	v_add_f32_dpp v2, v2, v2 row_shr:2 row_mask:0xf bank_mask:0xf bound_ctrl:1
	s_nop 1
	v_add_f32_dpp v2, v2, v2 row_shr:4 row_mask:0xf bank_mask:0xf bound_ctrl:1
	s_nop 1
	v_add_f32_dpp v2, v2, v2 row_shr:8 row_mask:0xf bank_mask:0xf bound_ctrl:1
	s_nop 1
	v_mov_b32_dpp v88, v2 row_bcast:15 row_mask:0xa bank_mask:0xf
	v_add_f32_e32 v2, v2, v88
	v_mov_b32_e32 v88, 0
	s_nop 1
	v_mov_b32_dpp v88, v2 row_bcast:31 row_mask:0xc bank_mask:0xf
	v_add_f32_e32 v2, v2, v88
	s_nop 0
	v_readlane_b32 s25, v2, 63
	s_nop 0
	s_waitcnt lgkmcnt(11)
	v_mul_f32_e32 v2, v87, v209
	ds_read_b128 v[204:207], v118 offset:28672
	v_fmac_f32_e32 v2, v86, v208
	v_mul_f32_e32 v88, v85, v211
	v_fmac_f32_e32 v88, v84, v210
	v_add_f32_e32 v2, v2, v88
	v_add_f32_e32 v2, 0, v2
	s_waitcnt lgkmcnt(11)
	v_mul_f32_e32 v89, v83, v213
	ds_read_b128 v[208:211], v118 offset:29696
	v_fmac_f32_e32 v89, v82, v212
	v_mul_f32_e32 v88, v81, v215
	v_fmac_f32_e32 v88, v80, v214
	v_add_f32_e32 v88, v89, v88
	v_add_f32_e32 v2, v2, v88
	s_waitcnt lgkmcnt(11)
; #define LAS __attribute__((address_space(3)))
; __device__ __forceinline__ float wave_sum(float v) { return lane63(scan64<false>(v)); }
; template <int YMODE, int EXTRA, bool NORM_OUT, bool XN8  , bool XIN_BF = false  , bool XOUT_BF = false  > ...
;     ...
;                     for (int e = 0; e < 8; ++e) { float s = 0.f;
; #pragma unroll
;                         for (int j = 0; j < 8; ++j) { const f32x4 w = *(const LAS f32x4*)(we + e * D + 256 * j + 4 * F.lane); s += (x[j][0] * w[0] + x[j][1] * w[1]) + (x[j][2] * w[2] + x[j][3] * w[3]); }
;                         d8[e] = wave_sum(s); asm volatile("" ::: "memory"); }
	v_mul_f32_e32 v89, v79, v217
	ds_read_b128 v[212:215], v118 offset:30720
	v_fmac_f32_e32 v89, v78, v216
	v_mul_f32_e32 v88, v77, v219
	v_fmac_f32_e32 v88, v76, v218
	v_add_f32_e32 v88, v89, v88
	v_add_f32_e32 v2, v2, v88
	s_waitcnt lgkmcnt(11)
	v_mul_f32_e32 v89, v75, v221
	ds_read_b128 v[216:219], v118 offset:31744
	v_fmac_f32_e32 v89, v74, v220
	v_mul_f32_e32 v88, v73, v223
	v_fmac_f32_e32 v88, v72, v222
	v_add_f32_e32 v88, v89, v88
	v_add_f32_e32 v2, v2, v88
	s_waitcnt lgkmcnt(11)
	v_mul_f32_e32 v89, v71, v225
	ds_read_b128 v[220:223], v118 offset:32768
	v_fmac_f32_e32 v89, v70, v224
	v_mul_f32_e32 v88, v69, v227
	v_fmac_f32_e32 v88, v68, v226
	v_add_f32_e32 v88, v89, v88
	v_add_f32_e32 v2, v2, v88
	s_waitcnt lgkmcnt(11)
	v_mul_f32_e32 v89, v67, v229
	ds_read_b128 v[224:227], v118 offset:33792
	v_fmac_f32_e32 v89, v66, v228
	v_mul_f32_e32 v88, v65, v231
	v_fmac_f32_e32 v88, v64, v230
	v_add_f32_e32 v88, v89, v88
	v_add_f32_e32 v2, v2, v88
	s_waitcnt lgkmcnt(11)
	v_mul_f32_e32 v89, v63, v233
	ds_read_b128 v[228:231], v118 offset:34816
	v_fmac_f32_e32 v89, v62, v232
	v_mul_f32_e32 v88, v61, v235
	v_fmac_f32_e32 v88, v60, v234
	v_add_f32_e32 v88, v89, v88
	v_add_f32_e32 v2, v2, v88
	s_waitcnt lgkmcnt(11)
	v_mul_f32_e32 v89, v59, v241
	ds_read_b128 v[232:235], v118 offset:35840
	v_fmac_f32_e32 v89, v58, v240
	v_mul_f32_e32 v88, v57, v243
	v_fmac_f32_e32 v88, v56, v242
	v_add_f32_e32 v88, v89, v88
	v_add_f32_e32 v2, v2, v88
	v_mov_b32_e32 v88, 0
	s_nop 0
	v_add_f32_dpp v2, v2, v2 row_shr:1 row_mask:0xf bank_mask:0xf bound_ctrl:1
	s_nop 1
	v_add_f32_dpp v2, v2, v2 row_shr:2 row_mask:0xf bank_mask:0xf bound_ctrl:1
	s_nop 1
	v_add_f32_dpp v2, v2, v2 row_shr:4 row_mask:0xf bank_mask:0xf bound_ctrl:1
	s_nop 1
	v_add_f32_dpp v2, v2, v2 row_shr:8 row_mask:0xf bank_mask:0xf bound_ctrl:1
	s_nop 1
	v_mov_b32_dpp v88, v2 row_bcast:15 row_mask:0xa bank_mask:0xf
	v_add_f32_e32 v2, v2, v88
	v_mov_b32_e32 v88, 0
	s_nop 1
	v_mov_b32_dpp v88, v2 row_bcast:31 row_mask:0xc bank_mask:0xf
	v_add_f32_e32 v2, v2, v88
	s_nop 0
	v_readlane_b32 s26, v2, 63
	s_nop 0
	s_waitcnt lgkmcnt(11)
	v_mul_f32_e32 v2, v87, v245
	ds_read_b128 v[240:243], v118 offset:36864
	v_fmac_f32_e32 v2, v86, v244
	v_mul_f32_e32 v88, v85, v247
	v_fmac_f32_e32 v88, v84, v246
	v_add_f32_e32 v2, v2, v88
	v_add_f32_e32 v2, 0, v2
	s_waitcnt lgkmcnt(11)
	v_mul_f32_e32 v89, v83, v249
	ds_read_b128 v[244:247], v118 offset:37888
	v_fmac_f32_e32 v89, v82, v248
	v_mul_f32_e32 v88, v81, v251
	v_fmac_f32_e32 v88, v80, v250
	v_add_f32_e32 v88, v89, v88
	v_add_f32_e32 v2, v2, v88
	s_waitcnt lgkmcnt(11)
	v_mul_f32_e32 v89, v79, v197
	ds_read_b128 v[248:251], v118 offset:38912
	v_fmac_f32_e32 v89, v78, v196
	v_mul_f32_e32 v88, v77, v199
	v_fmac_f32_e32 v88, v76, v198
	v_add_f32_e32 v88, v89, v88
	v_add_f32_e32 v2, v2, v88
	s_waitcnt lgkmcnt(11)
	v_mul_f32_e32 v89, v75, v201
	ds_read_b128 v[196:199], v118 offset:39936
	v_fmac_f32_e32 v89, v74, v200
	v_mul_f32_e32 v88, v73, v203
	v_fmac_f32_e32 v88, v72, v202
	v_add_f32_e32 v88, v89, v88
	v_add_f32_e32 v2, v2, v88
	s_waitcnt lgkmcnt(11)
	v_mul_f32_e32 v89, v71, v205
	ds_read_b128 v[200:203], v118 offset:40960
	v_fmac_f32_e32 v89, v70, v204
	v_mul_f32_e32 v88, v69, v207
	v_fmac_f32_e32 v88, v68, v206
	v_add_f32_e32 v88, v89, v88
	v_add_f32_e32 v2, v2, v88
	s_waitcnt lgkmcnt(11)
	v_mul_f32_e32 v89, v67, v209
	ds_read_b128 v[204:207], v118 offset:41984
	v_fmac_f32_e32 v89, v66, v208
	v_mul_f32_e32 v88, v65, v211
	v_fmac_f32_e32 v88, v64, v210
	v_add_f32_e32 v88, v89, v88
	v_add_f32_e32 v2, v2, v88
	s_waitcnt lgkmcnt(11)
	v_mul_f32_e32 v89, v63, v213
	ds_read_b128 v[208:211], v118 offset:43008
	v_fmac_f32_e32 v89, v62, v212
	v_mul_f32_e32 v88, v61, v215
	v_fmac_f32_e32 v88, v60, v214
	v_add_f32_e32 v88, v89, v88
	v_add_f32_e32 v2, v2, v88
	s_waitcnt lgkmcnt(11)
	v_mul_f32_e32 v89, v59, v217
	ds_read_b128 v[212:215], v118 offset:44032
	v_fmac_f32_e32 v89, v58, v216
	v_mul_f32_e32 v88, v57, v219
	v_fmac_f32_e32 v88, v56, v218
	v_add_f32_e32 v88, v89, v88
	v_add_f32_e32 v2, v2, v88
	v_mov_b32_e32 v88, 0
	s_nop 0
	v_add_f32_dpp v2, v2, v2 row_shr:1 row_mask:0xf bank_mask:0xf bound_ctrl:1
	s_nop 1
	v_add_f32_dpp v2, v2, v2 row_shr:2 row_mask:0xf bank_mask:0xf bound_ctrl:1
	s_nop 1
	v_add_f32_dpp v2, v2, v2 row_shr:4 row_mask:0xf bank_mask:0xf bound_ctrl:1
	s_nop 1
	v_add_f32_dpp v2, v2, v2 row_shr:8 row_mask:0xf bank_mask:0xf bound_ctrl:1
	s_nop 1
	v_mov_b32_dpp v88, v2 row_bcast:15 row_mask:0xa bank_mask:0xf
	v_add_f32_e32 v2, v2, v88
	v_mov_b32_e32 v88, 0
	s_nop 1
	v_mov_b32_dpp v88, v2 row_bcast:31 row_mask:0xc bank_mask:0xf
	v_add_f32_e32 v2, v2, v88
	s_nop 0
	v_readlane_b32 s27, v2, 63
	s_nop 0
	s_waitcnt lgkmcnt(11)
	v_mul_f32_e32 v2, v87, v221
	ds_read_b128 v[216:219], v118 offset:45056
	v_fmac_f32_e32 v2, v86, v220
	v_mul_f32_e32 v88, v85, v223
	v_fmac_f32_e32 v88, v84, v222
	v_add_f32_e32 v2, v2, v88
	v_add_f32_e32 v2, 0, v2
	s_waitcnt lgkmcnt(11)
	v_mul_f32_e32 v89, v83, v225
	ds_read_b128 v[220:223], v118 offset:46080
	v_fmac_f32_e32 v89, v82, v224
	v_mul_f32_e32 v88, v81, v227
	v_fmac_f32_e32 v88, v80, v226
	v_add_f32_e32 v88, v89, v88
	v_add_f32_e32 v2, v2, v88
	s_waitcnt lgkmcnt(11)
	v_mul_f32_e32 v89, v79, v229
	ds_read_b128 v[224:227], v118 offset:47104
	v_fmac_f32_e32 v89, v78, v228
	v_mul_f32_e32 v88, v77, v231
	v_fmac_f32_e32 v88, v76, v230
	v_add_f32_e32 v88, v89, v88
	v_add_f32_e32 v2, v2, v88
	s_waitcnt lgkmcnt(11)
	v_mul_f32_e32 v89, v75, v233
	ds_read_b128 v[228:231], v118 offset:48128
	v_fmac_f32_e32 v89, v74, v232
	v_mul_f32_e32 v88, v73, v235
	v_fmac_f32_e32 v88, v72, v234
	v_add_f32_e32 v88, v89, v88
	v_add_f32_e32 v2, v2, v88
	s_waitcnt lgkmcnt(11)
; #define LAS __attribute__((address_space(3)))
; __device__ __forceinline__ float wave_sum(float v) { return lane63(scan64<false>(v)); }
; template <int YMODE, int EXTRA, bool NORM_OUT, bool XN8  , bool XIN_BF = false  , bool XOUT_BF = false  > ...
;     ...
;                     for (int e = 0; e < 8; ++e) { float s = 0.f;
; #pragma unroll
;                         for (int j = 0; j < 8; ++j) { const f32x4 w = *(const LAS f32x4*)(we + e * D + 256 * j + 4 * F.lane); s += (x[j][0] * w[0] + x[j][1] * w[1]) + (x[j][2] * w[2] + x[j][3] * w[3]); }
;                         d8[e] = wave_sum(s); asm volatile("" ::: "memory"); }
	v_mul_f32_e32 v89, v71, v241
	ds_read_b128 v[232:235], v118 offset:49152
	v_fmac_f32_e32 v89, v70, v240
	v_mul_f32_e32 v88, v69, v243
	v_fmac_f32_e32 v88, v68, v242
	v_add_f32_e32 v88, v89, v88
	v_add_f32_e32 v2, v2, v88
	s_waitcnt lgkmcnt(11)
	v_mul_f32_e32 v89, v67, v245
	ds_read_b128 v[240:243], v118 offset:50176
	v_fmac_f32_e32 v89, v66, v244
	v_mul_f32_e32 v88, v65, v247
	v_fmac_f32_e32 v88, v64, v246
	v_add_f32_e32 v88, v89, v88
	v_add_f32_e32 v2, v2, v88
	s_waitcnt lgkmcnt(11)
	v_mul_f32_e32 v89, v63, v249
	ds_read_b128 v[244:247], v118 offset:51200
	v_fmac_f32_e32 v89, v62, v248
	v_mul_f32_e32 v88, v61, v251
	v_fmac_f32_e32 v88, v60, v250
	v_add_f32_e32 v88, v89, v88
	v_add_f32_e32 v2, v2, v88
	s_waitcnt lgkmcnt(11)
	v_mul_f32_e32 v89, v59, v197
	ds_read_b128 v[248:251], v118 offset:52224
	v_fmac_f32_e32 v89, v58, v196
	v_mul_f32_e32 v88, v57, v199
	v_fmac_f32_e32 v88, v56, v198
	v_add_f32_e32 v88, v89, v88
	v_add_f32_e32 v2, v2, v88
	v_mov_b32_e32 v88, 0
	s_nop 0
	v_add_f32_dpp v2, v2, v2 row_shr:1 row_mask:0xf bank_mask:0xf bound_ctrl:1
	s_nop 1
	v_add_f32_dpp v2, v2, v2 row_shr:2 row_mask:0xf bank_mask:0xf bound_ctrl:1
	s_nop 1
	v_add_f32_dpp v2, v2, v2 row_shr:4 row_mask:0xf bank_mask:0xf bound_ctrl:1
	s_nop 1
	v_add_f32_dpp v2, v2, v2 row_shr:8 row_mask:0xf bank_mask:0xf bound_ctrl:1
	s_nop 1
	v_mov_b32_dpp v88, v2 row_bcast:15 row_mask:0xa bank_mask:0xf
	v_add_f32_e32 v2, v2, v88
	v_mov_b32_e32 v88, 0
	s_nop 1
	v_mov_b32_dpp v88, v2 row_bcast:31 row_mask:0xc bank_mask:0xf
	v_add_f32_e32 v2, v2, v88
	s_nop 0
	v_readlane_b32 s78, v2, 63
	s_nop 0
	s_waitcnt lgkmcnt(11)
	v_mul_f32_e32 v2, v87, v201
	ds_read_b128 v[196:199], v118 offset:53248
	v_fmac_f32_e32 v2, v86, v200
	v_mul_f32_e32 v88, v85, v203
	v_fmac_f32_e32 v88, v84, v202
	v_add_f32_e32 v2, v2, v88
	v_add_f32_e32 v2, 0, v2
	s_waitcnt lgkmcnt(11)
	v_mul_f32_e32 v89, v83, v205
	ds_read_b128 v[200:203], v118 offset:54272
	v_fmac_f32_e32 v89, v82, v204
	v_mul_f32_e32 v88, v81, v207
	v_fmac_f32_e32 v88, v80, v206
	v_add_f32_e32 v88, v89, v88
	v_add_f32_e32 v2, v2, v88
	s_waitcnt lgkmcnt(11)
	v_mul_f32_e32 v89, v79, v209
	ds_read_b128 v[204:207], v118 offset:55296
	v_fmac_f32_e32 v89, v78, v208
	v_mul_f32_e32 v88, v77, v211
	v_fmac_f32_e32 v88, v76, v210
	v_add_f32_e32 v88, v89, v88
	v_add_f32_e32 v2, v2, v88
	s_waitcnt lgkmcnt(11)
	v_mul_f32_e32 v89, v75, v213
	ds_read_b128 v[208:211], v118 offset:56320
	v_fmac_f32_e32 v89, v74, v212
	v_mul_f32_e32 v88, v73, v215
	v_fmac_f32_e32 v88, v72, v214
	v_add_f32_e32 v88, v89, v88
	v_add_f32_e32 v2, v2, v88
	s_waitcnt lgkmcnt(11)
	v_mul_f32_e32 v89, v71, v217
	ds_read_b128 v[212:215], v118 offset:57344
	v_fmac_f32_e32 v89, v70, v216
	v_mul_f32_e32 v88, v69, v219
	v_fmac_f32_e32 v88, v68, v218
	v_add_f32_e32 v88, v89, v88
	v_add_f32_e32 v2, v2, v88
	s_waitcnt lgkmcnt(11)
	v_mul_f32_e32 v89, v67, v221
	ds_read_b128 v[216:219], v118 offset:58368
	v_fmac_f32_e32 v89, v66, v220
	v_mul_f32_e32 v88, v65, v223
	v_fmac_f32_e32 v88, v64, v222
	v_add_f32_e32 v88, v89, v88
	v_add_f32_e32 v2, v2, v88
	s_waitcnt lgkmcnt(11)
	v_mul_f32_e32 v89, v63, v225
	ds_read_b128 v[220:223], v118 offset:59392
	v_fmac_f32_e32 v89, v62, v224
	v_mul_f32_e32 v88, v61, v227
	v_fmac_f32_e32 v88, v60, v226
	v_add_f32_e32 v88, v89, v88
	v_add_f32_e32 v2, v2, v88
	s_waitcnt lgkmcnt(11)
	v_mul_f32_e32 v89, v59, v229
	ds_read_b128 v[224:227], v118 offset:60416
	v_fmac_f32_e32 v89, v58, v228
	v_mul_f32_e32 v88, v57, v231
	v_fmac_f32_e32 v88, v56, v230
	v_add_f32_e32 v88, v89, v88
	v_add_f32_e32 v2, v2, v88
	v_mov_b32_e32 v88, 0
	s_nop 0
	v_add_f32_dpp v2, v2, v2 row_shr:1 row_mask:0xf bank_mask:0xf bound_ctrl:1
	s_nop 1
	v_add_f32_dpp v2, v2, v2 row_shr:2 row_mask:0xf bank_mask:0xf bound_ctrl:1
	s_nop 1
	v_add_f32_dpp v2, v2, v2 row_shr:4 row_mask:0xf bank_mask:0xf bound_ctrl:1
	s_nop 1
	v_add_f32_dpp v2, v2, v2 row_shr:8 row_mask:0xf bank_mask:0xf bound_ctrl:1
	s_nop 1
	v_mov_b32_dpp v88, v2 row_bcast:15 row_mask:0xa bank_mask:0xf
	v_add_f32_e32 v2, v2, v88
	v_mov_b32_e32 v88, 0
	s_nop 1
	v_mov_b32_dpp v88, v2 row_bcast:31 row_mask:0xc bank_mask:0xf
	v_add_f32_e32 v2, v2, v88
	s_nop 0
	v_readlane_b32 s79, v2, 63
	s_nop 0
	s_waitcnt lgkmcnt(11)
	v_mul_f32_e32 v2, v87, v233
	ds_read_b128 v[228:231], v118 offset:61440
	v_fmac_f32_e32 v2, v86, v232
	v_mul_f32_e32 v88, v85, v235
	v_fmac_f32_e32 v88, v84, v234
	v_add_f32_e32 v2, v2, v88
	v_add_f32_e32 v2, 0, v2
	s_waitcnt lgkmcnt(11)
	v_mul_f32_e32 v89, v83, v241
	ds_read_b128 v[232:235], v118 offset:62464
	v_fmac_f32_e32 v89, v82, v240
	v_mul_f32_e32 v88, v81, v243
	v_fmac_f32_e32 v88, v80, v242
	v_add_f32_e32 v88, v89, v88
	v_add_f32_e32 v2, v2, v88
	s_waitcnt lgkmcnt(11)
	v_mul_f32_e32 v89, v79, v245
	ds_read_b128 v[240:243], v118 offset:63488
	v_fmac_f32_e32 v89, v78, v244
	v_mul_f32_e32 v88, v77, v247
	v_fmac_f32_e32 v88, v76, v246
	v_add_f32_e32 v88, v89, v88
	v_add_f32_e32 v2, v2, v88
	s_waitcnt lgkmcnt(11)
	v_mul_f32_e32 v89, v75, v249
	ds_read_b128 v[244:247], v118 offset:64512
	v_fmac_f32_e32 v89, v74, v248
	v_mul_f32_e32 v88, v73, v251
	v_fmac_f32_e32 v88, v72, v250
	v_add_f32_e32 v88, v89, v88
	v_add_f32_e32 v2, v2, v88
	s_waitcnt lgkmcnt(11)
	v_mul_f32_e32 v89, v71, v197
	v_fmac_f32_e32 v89, v70, v196
	v_mul_f32_e32 v88, v69, v199
	v_fmac_f32_e32 v88, v68, v198
	v_add_f32_e32 v88, v89, v88
	v_add_f32_e32 v2, v2, v88
	s_waitcnt lgkmcnt(10)
	v_mul_f32_e32 v89, v67, v201
	v_fmac_f32_e32 v89, v66, v200
	v_mul_f32_e32 v88, v65, v203
	v_fmac_f32_e32 v88, v64, v202
	v_add_f32_e32 v88, v89, v88
	v_add_f32_e32 v2, v2, v88
	s_waitcnt lgkmcnt(9)
; #define LAS __attribute__((address_space(3)))
; __device__ __forceinline__ float wave_sum(float v) { return lane63(scan64<false>(v)); }
; template <int YMODE, int EXTRA, bool NORM_OUT, bool XN8  , bool XIN_BF = false  , bool XOUT_BF = false  > ...
;     ...
;                     for (int e = 0; e < 8; ++e) { float s = 0.f;
; #pragma unroll
;                         for (int j = 0; j < 8; ++j) { const f32x4 w = *(const LAS f32x4*)(we + e * D + 256 * j + 4 * F.lane); s += (x[j][0] * w[0] + x[j][1] * w[1]) + (x[j][2] * w[2] + x[j][3] * w[3]); }
;                         d8[e] = wave_sum(s); asm volatile("" ::: "memory"); }
	v_mul_f32_e32 v89, v63, v205
	v_fmac_f32_e32 v89, v62, v204
	v_mul_f32_e32 v88, v61, v207
	v_fmac_f32_e32 v88, v60, v206
	v_add_f32_e32 v88, v89, v88
	v_add_f32_e32 v2, v2, v88
	s_waitcnt lgkmcnt(8)
	v_mul_f32_e32 v89, v59, v209
	v_fmac_f32_e32 v89, v58, v208
	v_mul_f32_e32 v88, v57, v211
	v_fmac_f32_e32 v88, v56, v210
	v_add_f32_e32 v88, v89, v88
	v_add_f32_e32 v2, v2, v88
	v_mov_b32_e32 v88, 0
	s_nop 0
	v_add_f32_dpp v2, v2, v2 row_shr:1 row_mask:0xf bank_mask:0xf bound_ctrl:1
	s_nop 1
	v_add_f32_dpp v2, v2, v2 row_shr:2 row_mask:0xf bank_mask:0xf bound_ctrl:1
	s_nop 1
	v_add_f32_dpp v2, v2, v2 row_shr:4 row_mask:0xf bank_mask:0xf bound_ctrl:1
	s_nop 1
	v_add_f32_dpp v2, v2, v2 row_shr:8 row_mask:0xf bank_mask:0xf bound_ctrl:1
	s_nop 1
	v_mov_b32_dpp v88, v2 row_bcast:15 row_mask:0xa bank_mask:0xf
	v_add_f32_e32 v2, v2, v88
	v_mov_b32_e32 v88, 0
	s_nop 1
	v_mov_b32_dpp v88, v2 row_bcast:31 row_mask:0xc bank_mask:0xf
	v_add_f32_e32 v2, v2, v88
	s_nop 0
	v_readlane_b32 s81, v2, 63
	s_nop 0
	s_waitcnt lgkmcnt(7)
	v_mul_f32_e32 v2, v87, v213
	v_mul_f32_e32 v85, v85, v215
	v_fmac_f32_e32 v2, v86, v212
	v_fmac_f32_e32 v85, v84, v214
	v_add_f32_e32 v2, v2, v85
	v_add_f32_e32 v2, 0, v2
	s_waitcnt lgkmcnt(6)
	v_mul_f32_e32 v83, v83, v217
	v_mul_f32_e32 v81, v81, v219
	v_fmac_f32_e32 v83, v82, v216
	v_fmac_f32_e32 v81, v80, v218
	v_add_f32_e32 v80, v83, v81
	v_add_f32_e32 v2, v2, v80
	s_waitcnt lgkmcnt(5)
	v_mul_f32_e32 v79, v79, v221
	v_mul_f32_e32 v77, v77, v223
	v_fmac_f32_e32 v79, v78, v220
	v_fmac_f32_e32 v77, v76, v222
	v_add_f32_e32 v76, v79, v77
	v_add_f32_e32 v2, v2, v76
	s_waitcnt lgkmcnt(4)
	v_mul_f32_e32 v75, v75, v225
	v_mul_f32_e32 v73, v73, v227
	v_fmac_f32_e32 v75, v74, v224
	v_fmac_f32_e32 v73, v72, v226
	v_add_f32_e32 v72, v75, v73
	v_add_f32_e32 v2, v2, v72
	s_waitcnt lgkmcnt(3)
	v_mul_f32_e32 v71, v71, v229
	v_mul_f32_e32 v69, v69, v231
	v_fmac_f32_e32 v71, v70, v228
	v_fmac_f32_e32 v69, v68, v230
	v_add_f32_e32 v68, v71, v69
	v_add_f32_e32 v2, v2, v68
	s_waitcnt lgkmcnt(2)
	v_mul_f32_e32 v67, v67, v233
	v_mul_f32_e32 v65, v65, v235
	v_fmac_f32_e32 v67, v66, v232
	v_fmac_f32_e32 v65, v64, v234
	v_add_f32_e32 v64, v67, v65
	v_add_f32_e32 v2, v2, v64
	s_waitcnt lgkmcnt(1)
	v_mul_f32_e32 v63, v63, v241
	v_mul_f32_e32 v61, v61, v243
	v_fmac_f32_e32 v63, v62, v240
	v_fmac_f32_e32 v61, v60, v242
	v_add_f32_e32 v60, v63, v61
	v_add_f32_e32 v2, v2, v60
	s_waitcnt lgkmcnt(0)
	v_mul_f32_e32 v59, v59, v245
	v_mul_f32_e32 v57, v57, v247
	v_fmac_f32_e32 v59, v58, v244
	v_fmac_f32_e32 v57, v56, v246
	v_add_f32_e32 v56, v59, v57
	v_add_f32_e32 v2, v2, v56
	v_mov_b32_e32 v56, 0
	s_nop 0
	v_add_f32_dpp v2, v2, v2 row_shr:1 row_mask:0xf bank_mask:0xf bound_ctrl:1
	s_nop 1
	v_add_f32_dpp v2, v2, v2 row_shr:2 row_mask:0xf bank_mask:0xf bound_ctrl:1
	s_nop 1
	v_add_f32_dpp v2, v2, v2 row_shr:4 row_mask:0xf bank_mask:0xf bound_ctrl:1
	s_nop 1
	v_add_f32_dpp v2, v2, v2 row_shr:8 row_mask:0xf bank_mask:0xf bound_ctrl:1
	s_nop 1
	v_mov_b32_dpp v56, v2 row_bcast:15 row_mask:0xa bank_mask:0xf
	v_add_f32_e32 v2, v2, v56
	v_mov_b32_e32 v56, 0
	s_nop 1
	v_mov_b32_dpp v56, v2 row_bcast:31 row_mask:0xc bank_mask:0xf
	v_add_f32_e32 v2, v2, v56
	s_nop 0
	v_readlane_b32 s82, v2, 63
	s_and_saveexec_b64 s[0:1], s[6:7]
	s_cbranch_execz .LBB0_2176
; template <int YMODE, int EXTRA, bool NORM_OUT, bool XN8  , bool XIN_BF = false  , bool XOUT_BF = false  > ...
;     ...
;                         int e1 = 0; float v1 = d8[0];
; #pragma unroll
;                         for (int e = 1; e < 8; ++e) if (d8[e] > v1) { v1 = d8[e]; e1 = e; }
;                         int e2 = -1; float v2 = -3.0e38f;
; #pragma unroll
;                         for (int e = 0; e < 8; ++e) if (e != e1 && d8[e] > v2) { v2 = d8[e]; e2 = e; }
;                         const float w1 = 1.f / (1.f + expf(v2 - v1));
;                         if (F.lane == 0) { routei[rl * 4 + 0] = e1; routei[rl * 4 + 1] = e2; route[rl * 4 + 2] = w1; route[rl * 4 + 3] = 1.f - w1; }
	v_mov_b32_e32 v2, s24
	v_cmp_gt_f32_e64 s[12:13], s25, v2
	v_mov_b32_e32 v56, s25
	v_mov_b32_e32 v58, s26
	v_cndmask_b32_e64 v57, v2, v56, s[12:13]
	v_cmp_gt_f32_e64 s[14:15], s26, v57
	v_mov_b32_e32 v59, s27
	v_mov_b32_e32 v60, s78
	v_cndmask_b32_e64 v57, v57, v58, s[14:15]
	v_cmp_gt_f32_e64 s[16:17], s27, v57
	v_mov_b32_e32 v61, s79
	v_mov_b32_e32 v62, s81
	v_cndmask_b32_e64 v57, v57, v59, s[16:17]
	v_cmp_gt_f32_e64 s[18:19], s78, v57
	v_cndmask_b32_e64 v63, 0, 1, s[12:13]
	s_nop 0
	v_cndmask_b32_e64 v57, v57, v60, s[18:19]
	v_cmp_gt_f32_e64 s[20:21], s79, v57
	s_nop 1
	v_cndmask_b32_e64 v57, v57, v61, s[20:21]
	v_cmp_gt_f32_e64 s[22:23], s81, v57
	s_nop 1
	v_cndmask_b32_e64 v57, v57, v62, s[22:23]
	v_cmp_ngt_f32_e32 vcc, s82, v57
	s_and_b64 s[84:85], s[22:23], vcc
	s_and_b64 s[12:13], s[14:15], exec
	v_readfirstlane_b32 s12, v63
	s_cselect_b32 s14, 2, s12
	s_and_b64 s[12:13], s[16:17], exec
	s_cselect_b32 s14, 3, s14
	s_and_b64 s[12:13], s[18:19], exec
	s_cselect_b32 s14, 4, s14
	s_and_b64 s[12:13], s[20:21], exec
	s_cselect_b32 s14, 5, s14
	s_and_b64 s[12:13], s[22:23], exec
	s_cselect_b32 s14, 6, s14
	s_and_b64 s[12:13], vcc, exec
	s_cselect_b32 s80, s14, 7
	s_cmp_lg_u32 s80, 5
	s_cselect_b64 s[86:87], -1, 0
	s_cmp_lg_u32 s80, 4
	s_cselect_b64 s[22:23], -1, 0
	s_cmp_lg_u32 s80, 3
	s_cselect_b64 s[20:21], -1, 0
	s_cmp_lg_u32 s80, 2
	s_cselect_b64 s[18:19], -1, 0
	s_cmp_lg_u32 s80, 1
	s_cselect_b64 s[16:17], -1, 0
	s_cmp_eq_u32 s80, 0
	s_cselect_b64 s[14:15], -1, 0
	v_cmp_ngt_f32_e64 s[12:13], s24, v126
	s_or_b64 s[12:13], s[12:13], s[14:15]
	s_nop 0
	v_cndmask_b32_e64 v2, v2, v126, s[12:13]
	v_cmp_gt_f32_e64 s[14:15], s25, v2
	s_and_b64 s[14:15], s[16:17], s[14:15]
	s_nop 0
	v_cndmask_b32_e64 v2, v2, v56, s[14:15]
	v_cmp_gt_f32_e64 s[16:17], s26, v2
	s_and_b64 s[16:17], s[18:19], s[16:17]
	v_mov_b32_e32 v56, s82
	v_cndmask_b32_e64 v2, v2, v58, s[16:17]
	v_cmp_gt_f32_e64 s[18:19], s27, v2
	s_and_b64 s[18:19], s[20:21], s[18:19]
	v_cndmask_b32_e64 v58, 0, -1, s[12:13]
	v_cndmask_b32_e64 v2, v2, v59, s[18:19]
	v_cmp_gt_f32_e64 s[20:21], s78, v2
	s_and_b64 s[20:21], s[22:23], s[20:21]
	s_nop 0
	v_cndmask_b32_e64 v2, v2, v60, s[20:21]
	v_cmp_gt_f32_e64 s[22:23], s79, v2
	s_and_b64 s[22:23], s[86:87], s[22:23]
	s_nop 0
	v_cndmask_b32_e64 v2, v2, v61, s[22:23]
	v_cmp_ngt_f32_e64 s[24:25], s81, v2
	s_or_b64 s[24:25], s[84:85], s[24:25]
	s_nop 0
	v_cndmask_b32_e64 v2, v62, v2, s[24:25]
	v_cmp_gt_f32_e64 s[26:27], s82, v2
	s_and_b64 s[26:27], vcc, s[26:27]
	s_and_b64 s[12:13], s[14:15], exec
	v_readfirstlane_b32 s12, v58
	s_cselect_b32 s14, 1, s12
	s_and_b64 s[12:13], s[16:17], exec
	s_cselect_b32 s14, 2, s14
	s_and_b64 s[12:13], s[18:19], exec
	s_cselect_b32 s14, 3, s14
	s_and_b64 s[12:13], s[20:21], exec
	s_cselect_b32 s14, 4, s14
	s_and_b64 s[12:13], s[22:23], exec
	v_cndmask_b32_e64 v2, v2, v56, s[26:27]
	s_cselect_b32 s14, 5, s14
	s_and_b64 s[12:13], s[24:25], exec
	v_cndmask_b32_e32 v56, v56, v57, vcc
	s_cselect_b32 s14, s14, 6
	s_and_b64 s[12:13], s[26:27], exec
	v_sub_f32_e32 v2, v2, v56
	v_mul_f32_e32 v56, 0x3fb8aa3b, v2
	s_mov_b32 s13, 0x3fb8aa3b
	v_fma_f32 v57, v2, s13, -v56
	v_rndne_f32_e32 v58, v56
	v_fmac_f32_e32 v57, 0x32a5705f, v2
	v_sub_f32_e32 v56, v56, v58
	v_add_f32_e32 v56, v56, v57
	v_exp_f32_e32 v56, v56
	v_cvt_i32_f32_e32 v57, v58
	s_mov_b32 s13, 0xc2ce8ed0
	v_cmp_ngt_f32_e32 vcc, s13, v2
	s_mov_b32 s13, 0x42b17218
	v_ldexp_f32 v56, v56, v57
	v_cndmask_b32_e32 v56, 0, v56, vcc
	v_cmp_nlt_f32_e32 vcc, s13, v2
	s_cselect_b32 s12, 7, s14
	s_lshl_b32 s13, s42, 4
	v_cndmask_b32_e32 v2, v127, v56, vcc
	v_add_f32_e32 v2, 1.0, v2
	v_div_scale_f32 v56, s[14:15], v2, v2, 1.0
	v_rcp_f32_e32 v57, v56
	s_add_i32 s13, s13, 0
	s_add_i32 s13, s13, 0x16000
	v_fma_f32 v58, -v56, v57, 1.0
	v_fmac_f32_e32 v57, v58, v57
	v_div_scale_f32 v58, vcc, 1.0, v2, 1.0
	v_mul_f32_e32 v59, v58, v57
	v_fma_f32 v60, -v56, v59, v58
	v_fmac_f32_e32 v59, v60, v57
	v_fma_f32 v56, -v56, v59, v58
	v_div_fmas_f32 v56, v56, v57, v59
	v_div_fixup_f32 v58, v56, v2, 1.0
	v_sub_f32_e32 v59, 1.0, v58
	v_mov_b32_e32 v56, s80
	v_mov_b32_e32 v57, s12
	v_mov_b32_e32 v2, s13
	ds_write_b128 v2, v[56:59]
	s_branch .LBB0_2176
